# vK
# baseline (speedup 1.0000x reference)
.Lsp_skip:
	s_or_b64 exec, exec, s[36:37]
	v_mov_b32_e32 v244, v245
	v_mov_b32_e32 v245, v3
	s_add_u32 s58, s58, 1
	s_cmp_lt_u32 s58, 2
	s_cbranch_scc1 .Lsp_loop
	s_waitcnt vmcnt(21)
	v_cvt_pk_f16_f32 v204, v204, v205
	v_cvt_pk_f16_f32 v205, v206, v207
	ds_write_b64 v237, v[204:205]
	s_waitcnt vmcnt(20)
	v_cvt_pk_f16_f32 v208, v208, v209
	v_cvt_pk_f16_f32 v209, v210, v211
	ds_write_b64 v237, v[208:209] offset:4352
	s_waitcnt vmcnt(19)
	v_cvt_pk_f16_f32 v212, v212, v213
	v_cvt_pk_f16_f32 v213, v214, v215
	ds_write_b64 v237, v[212:213] offset:8704
	s_waitcnt vmcnt(18)
	v_cvt_pk_f16_f32 v216, v216, v217
	v_cvt_pk_f16_f32 v217, v218, v219
	ds_write_b64 v237, v[216:217] offset:13056
	s_waitcnt vmcnt(17)
	v_cvt_pk_f16_f32 v220, v220, v221
	v_cvt_pk_f16_f32 v221, v222, v223
	ds_write_b64 v237, v[220:221] offset:17408
	s_waitcnt vmcnt(16)
	v_cvt_pk_f16_f32 v224, v224, v225
	v_cvt_pk_f16_f32 v225, v226, v227
	ds_write_b64 v237, v[224:225] offset:21760
	s_waitcnt vmcnt(15)
	v_cvt_pk_f16_f32 v228, v228, v229
	v_cvt_pk_f16_f32 v229, v230, v231
	ds_write_b64 v237, v[228:229] offset:26112
	s_waitcnt vmcnt(14)
	v_cvt_pk_f16_f32 v232, v232, v233
	v_cvt_pk_f16_f32 v233, v234, v235
	ds_write_b64 v237, v[232:233] offset:30464
	global_load_dwordx4 v[204:207], v238, s[40:41] offset:512 nt
	global_load_dwordx4 v[208:211], v238, s[42:43] offset:512 nt
	global_load_dwordx4 v[212:215], v238, s[44:45] offset:512 nt
	global_load_dwordx4 v[216:219], v238, s[46:47] offset:512 nt
	global_load_dwordx4 v[220:223], v238, s[48:49] offset:512 nt
	global_load_dwordx4 v[224:227], v238, s[50:51] offset:512 nt
	global_load_dwordx4 v[228:231], v238, s[52:53] offset:512 nt
	global_load_dwordx4 v[232:235], v238, s[54:55] offset:512 nt
	s_waitcnt lgkmcnt(0)
	s_barrier
	ds_read_b128 v[130:133], v236
	ds_read_b128 v[134:137], v236 offset:4352
	ds_read_b128 v[138:141], v236 offset:8704
	ds_read_b128 v[142:145], v236 offset:13056
	s_waitcnt vmcnt(20)
	s_waitcnt lgkmcnt(3)
	v_mfma_f32_32x32x16_f16 v[82:97], v[130:133], v[146:149], 0
	v_mfma_f32_32x32x16_f16 v[50:65], v[130:133], v[150:153], 0
	ds_read_b128 v[130:133], v236 offset:32
	s_waitcnt lgkmcnt(3)
	v_mfma_f32_32x32x16_f16 v[114:129], v[134:137], v[146:149], 0
	v_mfma_f32_32x32x16_f16 v[34:49], v[134:137], v[150:153], 0
	ds_read_b128 v[134:137], v236 offset:4384
	s_waitcnt lgkmcnt(3)
	v_mfma_f32_32x32x16_f16 v[98:113], v[138:141], v[146:149], 0
	v_mfma_f32_32x32x16_f16 v[18:33], v[138:141], v[150:153], 0
	ds_read_b128 v[138:141], v236 offset:8736
	s_waitcnt lgkmcnt(3)
	v_mfma_f32_32x32x16_f16 v[66:81], v[142:145], v[146:149], 0
	v_mfma_f32_32x32x16_f16 v[2:17], v[142:145], v[150:153], 0
	ds_read_b128 v[142:145], v236 offset:13088
	global_load_dwordx4 v[146:149], v239, s[56:57]
	global_load_dwordx4 v[150:153], v239, s[56:57] offset:512
	s_add_u32 s56, s56, 0x4000
	s_addc_u32 s57, s57, 0
	s_waitcnt vmcnt(20)
	s_waitcnt lgkmcnt(3)
	v_mfma_f32_32x32x16_f16 v[82:97], v[130:133], v[154:157], v[82:97]
	v_mfma_f32_32x32x16_f16 v[50:65], v[130:133], v[158:161], v[50:65]
	ds_read_b128 v[130:133], v236 offset:64
	s_waitcnt lgkmcnt(3)
	v_mfma_f32_32x32x16_f16 v[114:129], v[134:137], v[154:157], v[114:129]
	v_mfma_f32_32x32x16_f16 v[34:49], v[134:137], v[158:161], v[34:49]
	ds_read_b128 v[134:137], v236 offset:4416
	s_waitcnt lgkmcnt(3)
	v_mfma_f32_32x32x16_f16 v[98:113], v[138:141], v[154:157], v[98:113]
	v_mfma_f32_32x32x16_f16 v[18:33], v[138:141], v[158:161], v[18:33]
	ds_read_b128 v[138:141], v236 offset:8768
	s_waitcnt lgkmcnt(3)
	v_mfma_f32_32x32x16_f16 v[66:81], v[142:145], v[154:157], v[66:81]
	v_mfma_f32_32x32x16_f16 v[2:17], v[142:145], v[158:161], v[2:17]
	ds_read_b128 v[142:145], v236 offset:13120
	global_load_dwordx4 v[154:157], v239, s[56:57]
	global_load_dwordx4 v[158:161], v239, s[56:57] offset:512
	s_add_u32 s56, s56, 0x4000
	s_addc_u32 s57, s57, 0
	s_waitcnt vmcnt(20)
	s_waitcnt lgkmcnt(3)
	v_mfma_f32_32x32x16_f16 v[82:97], v[130:133], v[162:165], v[82:97]
	v_mfma_f32_32x32x16_f16 v[50:65], v[130:133], v[166:169], v[50:65]
	ds_read_b128 v[130:133], v236 offset:96
	s_waitcnt lgkmcnt(3)
	v_mfma_f32_32x32x16_f16 v[114:129], v[134:137], v[162:165], v[114:129]
	v_mfma_f32_32x32x16_f16 v[34:49], v[134:137], v[166:169], v[34:49]
	ds_read_b128 v[134:137], v236 offset:4448
	s_waitcnt lgkmcnt(3)
	v_mfma_f32_32x32x16_f16 v[98:113], v[138:141], v[162:165], v[98:113]
	v_mfma_f32_32x32x16_f16 v[18:33], v[138:141], v[166:169], v[18:33]
	ds_read_b128 v[138:141], v236 offset:8800
	s_waitcnt lgkmcnt(3)
	v_mfma_f32_32x32x16_f16 v[66:81], v[142:145], v[162:165], v[66:81]
	v_mfma_f32_32x32x16_f16 v[2:17], v[142:145], v[166:169], v[2:17]
	ds_read_b128 v[142:145], v236 offset:13152
	global_load_dwordx4 v[162:165], v239, s[56:57]
	global_load_dwordx4 v[166:169], v239, s[56:57] offset:512
	s_add_u32 s56, s56, 0x4000
	s_addc_u32 s57, s57, 0
	s_waitcnt vmcnt(20)
	s_waitcnt lgkmcnt(3)
	v_mfma_f32_32x32x16_f16 v[82:97], v[130:133], v[170:173], v[82:97]
	v_mfma_f32_32x32x16_f16 v[50:65], v[130:133], v[174:177], v[50:65]
	ds_read_b128 v[130:133], v236 offset:128
	s_waitcnt lgkmcnt(3)
	v_mfma_f32_32x32x16_f16 v[114:129], v[134:137], v[170:173], v[114:129]
	v_mfma_f32_32x32x16_f16 v[34:49], v[134:137], v[174:177], v[34:49]
	ds_read_b128 v[134:137], v236 offset:4480
	s_waitcnt lgkmcnt(3)
	v_mfma_f32_32x32x16_f16 v[98:113], v[138:141], v[170:173], v[98:113]
	v_mfma_f32_32x32x16_f16 v[18:33], v[138:141], v[174:177], v[18:33]
	ds_read_b128 v[138:141], v236 offset:8832
	s_waitcnt lgkmcnt(3)
	v_mfma_f32_32x32x16_f16 v[66:81], v[142:145], v[170:173], v[66:81]
	v_mfma_f32_32x32x16_f16 v[2:17], v[142:145], v[174:177], v[2:17]
	ds_read_b128 v[142:145], v236 offset:13184
	global_load_dwordx4 v[170:173], v239, s[56:57]
	global_load_dwordx4 v[174:177], v239, s[56:57] offset:512
	s_add_u32 s56, s56, 0x4000
	s_addc_u32 s57, s57, 0
	s_waitcnt vmcnt(20)
	s_waitcnt lgkmcnt(3)
	v_mfma_f32_32x32x16_f16 v[82:97], v[130:133], v[178:181], v[82:97]
	v_mfma_f32_32x32x16_f16 v[50:65], v[130:133], v[182:185], v[50:65]
	ds_read_b128 v[130:133], v236 offset:160
	s_waitcnt lgkmcnt(3)
	v_mfma_f32_32x32x16_f16 v[114:129], v[134:137], v[178:181], v[114:129]
	v_mfma_f32_32x32x16_f16 v[34:49], v[134:137], v[182:185], v[34:49]
	ds_read_b128 v[134:137], v236 offset:4512
	s_waitcnt lgkmcnt(3)
	v_mfma_f32_32x32x16_f16 v[98:113], v[138:141], v[178:181], v[98:113]
	v_mfma_f32_32x32x16_f16 v[18:33], v[138:141], v[182:185], v[18:33]
	ds_read_b128 v[138:141], v236 offset:8864
	s_waitcnt lgkmcnt(3)
	v_mfma_f32_32x32x16_f16 v[66:81], v[142:145], v[178:181], v[66:81]
	v_mfma_f32_32x32x16_f16 v[2:17], v[142:145], v[182:185], v[2:17]
	ds_read_b128 v[142:145], v236 offset:13216
	global_load_dwordx4 v[178:181], v239, s[56:57]
	global_load_dwordx4 v[182:185], v239, s[56:57] offset:512
	s_add_u32 s56, s56, 0x4000
	s_addc_u32 s57, s57, 0
	s_waitcnt vmcnt(20)
	s_waitcnt lgkmcnt(3)
	v_mfma_f32_32x32x16_f16 v[82:97], v[130:133], v[186:189], v[82:97]
	v_mfma_f32_32x32x16_f16 v[50:65], v[130:133], v[190:193], v[50:65]
	ds_read_b128 v[130:133], v236 offset:192
	s_waitcnt lgkmcnt(3)
	v_mfma_f32_32x32x16_f16 v[114:129], v[134:137], v[186:189], v[114:129]
	v_mfma_f32_32x32x16_f16 v[34:49], v[134:137], v[190:193], v[34:49]
	ds_read_b128 v[134:137], v236 offset:4544
	s_waitcnt lgkmcnt(3)
	v_mfma_f32_32x32x16_f16 v[98:113], v[138:141], v[186:189], v[98:113]
	v_mfma_f32_32x32x16_f16 v[18:33], v[138:141], v[190:193], v[18:33]
	ds_read_b128 v[138:141], v236 offset:8896
	s_waitcnt lgkmcnt(3)
	v_mfma_f32_32x32x16_f16 v[66:81], v[142:145], v[186:189], v[66:81]
	v_mfma_f32_32x32x16_f16 v[2:17], v[142:145], v[190:193], v[2:17]
	ds_read_b128 v[142:145], v236 offset:13248
	global_load_dwordx4 v[186:189], v239, s[56:57]
	global_load_dwordx4 v[190:193], v239, s[56:57] offset:512
	s_add_u32 s56, s56, 0x4000
	s_addc_u32 s57, s57, 0
	s_waitcnt vmcnt(19)
	v_cvt_pk_f16_f32 v204, v204, v205
	v_cvt_pk_f16_f32 v205, v206, v207
	ds_write_b64 v237, v[204:205] offset:34816
	s_waitcnt vmcnt(18)
	v_cvt_pk_f16_f32 v208, v208, v209
	v_cvt_pk_f16_f32 v209, v210, v211
	ds_write_b64 v237, v[208:209] offset:39168
	s_waitcnt vmcnt(17)
	v_cvt_pk_f16_f32 v212, v212, v213
	v_cvt_pk_f16_f32 v213, v214, v215
	ds_write_b64 v237, v[212:213] offset:43520
	s_waitcnt vmcnt(16)
	v_cvt_pk_f16_f32 v216, v216, v217
	v_cvt_pk_f16_f32 v217, v218, v219
	ds_write_b64 v237, v[216:217] offset:47872
	s_waitcnt vmcnt(15)
	v_cvt_pk_f16_f32 v220, v220, v221
	v_cvt_pk_f16_f32 v221, v222, v223
	ds_write_b64 v237, v[220:221] offset:52224
	s_waitcnt vmcnt(14)
	v_cvt_pk_f16_f32 v224, v224, v225
	v_cvt_pk_f16_f32 v225, v226, v227
	ds_write_b64 v237, v[224:225] offset:56576
	s_waitcnt vmcnt(13)
	v_cvt_pk_f16_f32 v228, v228, v229
	v_cvt_pk_f16_f32 v229, v230, v231
	ds_write_b64 v237, v[228:229] offset:60928
	s_waitcnt vmcnt(12)
	v_cvt_pk_f16_f32 v232, v232, v233
	v_cvt_pk_f16_f32 v233, v234, v235
	ds_write_b64 v237, v[232:233] offset:65280
	global_load_dwordx4 v[204:207], v238, s[40:41] offset:1024 nt
	global_load_dwordx4 v[208:211], v238, s[42:43] offset:1024 nt
	global_load_dwordx4 v[212:215], v238, s[44:45] offset:1024 nt
	global_load_dwordx4 v[216:219], v238, s[46:47] offset:1024 nt
	global_load_dwordx4 v[220:223], v238, s[48:49] offset:1024 nt
	global_load_dwordx4 v[224:227], v238, s[50:51] offset:1024 nt
	global_load_dwordx4 v[228:231], v238, s[52:53] offset:1024 nt
	global_load_dwordx4 v[232:235], v238, s[54:55] offset:1024 nt
	s_waitcnt vmcnt(28)
	s_waitcnt lgkmcnt(11)
	v_mfma_f32_32x32x16_f16 v[82:97], v[130:133], v[194:197], v[82:97]
	v_mfma_f32_32x32x16_f16 v[50:65], v[130:133], v[198:201], v[50:65]
	ds_read_b128 v[130:133], v236 offset:224
	s_waitcnt lgkmcnt(11)
	v_mfma_f32_32x32x16_f16 v[114:129], v[134:137], v[194:197], v[114:129]
	v_mfma_f32_32x32x16_f16 v[34:49], v[134:137], v[198:201], v[34:49]
	ds_read_b128 v[134:137], v236 offset:4576
	s_waitcnt lgkmcnt(11)
	v_mfma_f32_32x32x16_f16 v[98:113], v[138:141], v[194:197], v[98:113]
	v_mfma_f32_32x32x16_f16 v[18:33], v[138:141], v[198:201], v[18:33]
	ds_read_b128 v[138:141], v236 offset:8928
	s_waitcnt lgkmcnt(11)
	v_mfma_f32_32x32x16_f16 v[66:81], v[142:145], v[194:197], v[66:81]
	v_mfma_f32_32x32x16_f16 v[2:17], v[142:145], v[198:201], v[2:17]
	ds_read_b128 v[142:145], v236 offset:13280
	global_load_dwordx4 v[194:197], v239, s[56:57]
	global_load_dwordx4 v[198:201], v239, s[56:57] offset:512
	s_add_u32 s56, s56, 0x4000
	s_addc_u32 s57, s57, 0
	s_waitcnt vmcnt(20)
	s_waitcnt lgkmcnt(3)
	v_mfma_f32_32x32x16_f16 v[82:97], v[130:133], v[146:149], v[82:97]
	v_mfma_f32_32x32x16_f16 v[50:65], v[130:133], v[150:153], v[50:65]
	s_waitcnt lgkmcnt(2)
	v_mfma_f32_32x32x16_f16 v[114:129], v[134:137], v[146:149], v[114:129]
	v_mfma_f32_32x32x16_f16 v[34:49], v[134:137], v[150:153], v[34:49]
	s_waitcnt lgkmcnt(1)
	v_mfma_f32_32x32x16_f16 v[98:113], v[138:141], v[146:149], v[98:113]
	v_mfma_f32_32x32x16_f16 v[18:33], v[138:141], v[150:153], v[18:33]
	s_waitcnt lgkmcnt(0)
	v_mfma_f32_32x32x16_f16 v[66:81], v[142:145], v[146:149], v[66:81]
	v_mfma_f32_32x32x16_f16 v[2:17], v[142:145], v[150:153], v[2:17]
	global_load_dwordx4 v[146:149], v239, s[56:57]
	global_load_dwordx4 v[150:153], v239, s[56:57] offset:512
	s_add_u32 s56, s56, 0x4000
	s_addc_u32 s57, s57, 0
	s_waitcnt lgkmcnt(0)
	s_barrier
	ds_read_b128 v[130:133], v236 offset:34816
	ds_read_b128 v[134:137], v236 offset:39168
	ds_read_b128 v[138:141], v236 offset:43520
	ds_read_b128 v[142:145], v236 offset:47872
	s_waitcnt vmcnt(20)
	s_waitcnt lgkmcnt(3)
	v_mfma_f32_32x32x16_f16 v[82:97], v[130:133], v[154:157], v[82:97]
	v_mfma_f32_32x32x16_f16 v[50:65], v[130:133], v[158:161], v[50:65]
	ds_read_b128 v[130:133], v236 offset:34848
	s_waitcnt lgkmcnt(3)
	v_mfma_f32_32x32x16_f16 v[114:129], v[134:137], v[154:157], v[114:129]
	v_mfma_f32_32x32x16_f16 v[34:49], v[134:137], v[158:161], v[34:49]
	ds_read_b128 v[134:137], v236 offset:39200
	s_waitcnt lgkmcnt(3)
	v_mfma_f32_32x32x16_f16 v[98:113], v[138:141], v[154:157], v[98:113]
	v_mfma_f32_32x32x16_f16 v[18:33], v[138:141], v[158:161], v[18:33]
	ds_read_b128 v[138:141], v236 offset:43552
	s_waitcnt lgkmcnt(3)
	v_mfma_f32_32x32x16_f16 v[66:81], v[142:145], v[154:157], v[66:81]
	v_mfma_f32_32x32x16_f16 v[2:17], v[142:145], v[158:161], v[2:17]
	ds_read_b128 v[142:145], v236 offset:47904
	global_load_dwordx4 v[154:157], v239, s[56:57]
	global_load_dwordx4 v[158:161], v239, s[56:57] offset:512
	s_add_u32 s56, s56, 0x4000
	s_addc_u32 s57, s57, 0
	s_waitcnt vmcnt(20)
	s_waitcnt lgkmcnt(3)
	v_mfma_f32_32x32x16_f16 v[82:97], v[130:133], v[162:165], v[82:97]
	v_mfma_f32_32x32x16_f16 v[50:65], v[130:133], v[166:169], v[50:65]
	ds_read_b128 v[130:133], v236 offset:34880
	s_waitcnt lgkmcnt(3)
	v_mfma_f32_32x32x16_f16 v[114:129], v[134:137], v[162:165], v[114:129]
	v_mfma_f32_32x32x16_f16 v[34:49], v[134:137], v[166:169], v[34:49]
	ds_read_b128 v[134:137], v236 offset:39232
	s_waitcnt lgkmcnt(3)
	v_mfma_f32_32x32x16_f16 v[98:113], v[138:141], v[162:165], v[98:113]
	v_mfma_f32_32x32x16_f16 v[18:33], v[138:141], v[166:169], v[18:33]
	ds_read_b128 v[138:141], v236 offset:43584
	s_waitcnt lgkmcnt(3)
	v_mfma_f32_32x32x16_f16 v[66:81], v[142:145], v[162:165], v[66:81]
	v_mfma_f32_32x32x16_f16 v[2:17], v[142:145], v[166:169], v[2:17]
	ds_read_b128 v[142:145], v236 offset:47936
	global_load_dwordx4 v[162:165], v239, s[56:57]
	global_load_dwordx4 v[166:169], v239, s[56:57] offset:512
	s_add_u32 s56, s56, 0x4000
	s_addc_u32 s57, s57, 0
	s_waitcnt vmcnt(20)
	s_waitcnt lgkmcnt(3)
	v_mfma_f32_32x32x16_f16 v[82:97], v[130:133], v[170:173], v[82:97]
	v_mfma_f32_32x32x16_f16 v[50:65], v[130:133], v[174:177], v[50:65]
	ds_read_b128 v[130:133], v236 offset:34912
	s_waitcnt lgkmcnt(3)
	v_mfma_f32_32x32x16_f16 v[114:129], v[134:137], v[170:173], v[114:129]
	v_mfma_f32_32x32x16_f16 v[34:49], v[134:137], v[174:177], v[34:49]
	ds_read_b128 v[134:137], v236 offset:39264
	s_waitcnt lgkmcnt(3)
	v_mfma_f32_32x32x16_f16 v[98:113], v[138:141], v[170:173], v[98:113]
	v_mfma_f32_32x32x16_f16 v[18:33], v[138:141], v[174:177], v[18:33]
	ds_read_b128 v[138:141], v236 offset:43616
	s_waitcnt lgkmcnt(3)
	v_mfma_f32_32x32x16_f16 v[66:81], v[142:145], v[170:173], v[66:81]
	v_mfma_f32_32x32x16_f16 v[2:17], v[142:145], v[174:177], v[2:17]
	ds_read_b128 v[142:145], v236 offset:47968
	global_load_dwordx4 v[170:173], v239, s[56:57]
	global_load_dwordx4 v[174:177], v239, s[56:57] offset:512
	s_add_u32 s56, s56, 0x4000
	s_addc_u32 s57, s57, 0
	s_waitcnt vmcnt(20)
	s_waitcnt lgkmcnt(3)
	v_mfma_f32_32x32x16_f16 v[82:97], v[130:133], v[178:181], v[82:97]
	v_mfma_f32_32x32x16_f16 v[50:65], v[130:133], v[182:185], v[50:65]
	ds_read_b128 v[130:133], v236 offset:34944
	s_waitcnt lgkmcnt(3)
	v_mfma_f32_32x32x16_f16 v[114:129], v[134:137], v[178:181], v[114:129]
	v_mfma_f32_32x32x16_f16 v[34:49], v[134:137], v[182:185], v[34:49]
	ds_read_b128 v[134:137], v236 offset:39296
	s_waitcnt lgkmcnt(3)
	v_mfma_f32_32x32x16_f16 v[98:113], v[138:141], v[178:181], v[98:113]
	v_mfma_f32_32x32x16_f16 v[18:33], v[138:141], v[182:185], v[18:33]
	ds_read_b128 v[138:141], v236 offset:43648
	s_waitcnt lgkmcnt(3)
	v_mfma_f32_32x32x16_f16 v[66:81], v[142:145], v[178:181], v[66:81]
	v_mfma_f32_32x32x16_f16 v[2:17], v[142:145], v[182:185], v[2:17]
	ds_read_b128 v[142:145], v236 offset:48000
	global_load_dwordx4 v[178:181], v239, s[56:57]
	global_load_dwordx4 v[182:185], v239, s[56:57] offset:512
	s_add_u32 s56, s56, 0x4000
	s_addc_u32 s57, s57, 0
	s_waitcnt vmcnt(20)
	s_waitcnt lgkmcnt(3)
	v_mfma_f32_32x32x16_f16 v[82:97], v[130:133], v[186:189], v[82:97]
	v_mfma_f32_32x32x16_f16 v[50:65], v[130:133], v[190:193], v[50:65]
	ds_read_b128 v[130:133], v236 offset:34976
	s_waitcnt lgkmcnt(3)
	v_mfma_f32_32x32x16_f16 v[114:129], v[134:137], v[186:189], v[114:129]
	v_mfma_f32_32x32x16_f16 v[34:49], v[134:137], v[190:193], v[34:49]
	ds_read_b128 v[134:137], v236 offset:39328
	s_waitcnt lgkmcnt(3)
	v_mfma_f32_32x32x16_f16 v[98:113], v[138:141], v[186:189], v[98:113]
	v_mfma_f32_32x32x16_f16 v[18:33], v[138:141], v[190:193], v[18:33]
	ds_read_b128 v[138:141], v236 offset:43680
	s_waitcnt lgkmcnt(3)
	v_mfma_f32_32x32x16_f16 v[66:81], v[142:145], v[186:189], v[66:81]
	v_mfma_f32_32x32x16_f16 v[2:17], v[142:145], v[190:193], v[2:17]
	ds_read_b128 v[142:145], v236 offset:48032
	global_load_dwordx4 v[186:189], v239, s[56:57]
	global_load_dwordx4 v[190:193], v239, s[56:57] offset:512
	s_add_u32 s56, s56, 0x4000
	s_addc_u32 s57, s57, 0
	s_waitcnt vmcnt(12)
	s_waitcnt lgkmcnt(3)
	v_mfma_f32_32x32x16_f16 v[82:97], v[130:133], v[194:197], v[82:97]
	v_mfma_f32_32x32x16_f16 v[50:65], v[130:133], v[198:201], v[50:65]
	ds_read_b128 v[130:133], v236 offset:35008
	s_waitcnt lgkmcnt(3)
	v_mfma_f32_32x32x16_f16 v[114:129], v[134:137], v[194:197], v[114:129]
	v_mfma_f32_32x32x16_f16 v[34:49], v[134:137], v[198:201], v[34:49]
	ds_read_b128 v[134:137], v236 offset:39360
	s_waitcnt lgkmcnt(3)
	v_mfma_f32_32x32x16_f16 v[98:113], v[138:141], v[194:197], v[98:113]
	v_mfma_f32_32x32x16_f16 v[18:33], v[138:141], v[198:201], v[18:33]
	ds_read_b128 v[138:141], v236 offset:43712
	s_waitcnt lgkmcnt(3)
	v_mfma_f32_32x32x16_f16 v[66:81], v[142:145], v[194:197], v[66:81]
	v_mfma_f32_32x32x16_f16 v[2:17], v[142:145], v[198:201], v[2:17]
	ds_read_b128 v[142:145], v236 offset:48064
	global_load_dwordx4 v[194:197], v239, s[56:57]
	global_load_dwordx4 v[198:201], v239, s[56:57] offset:512
	s_add_u32 s56, s56, 0x4000
	s_addc_u32 s57, s57, 0
	s_waitcnt vmcnt(23)
	v_cvt_pk_f16_f32 v204, v204, v205
	v_cvt_pk_f16_f32 v205, v206, v207
	ds_write_b64 v237, v[204:205]
	s_waitcnt vmcnt(22)
	v_cvt_pk_f16_f32 v208, v208, v209
	v_cvt_pk_f16_f32 v209, v210, v211
	ds_write_b64 v237, v[208:209] offset:4352
	s_waitcnt vmcnt(21)
	v_cvt_pk_f16_f32 v212, v212, v213
	v_cvt_pk_f16_f32 v213, v214, v215
	ds_write_b64 v237, v[212:213] offset:8704
	s_waitcnt vmcnt(20)
	v_cvt_pk_f16_f32 v216, v216, v217
	v_cvt_pk_f16_f32 v217, v218, v219
	ds_write_b64 v237, v[216:217] offset:13056
	s_waitcnt vmcnt(19)
	v_cvt_pk_f16_f32 v220, v220, v221
	v_cvt_pk_f16_f32 v221, v222, v223
	ds_write_b64 v237, v[220:221] offset:17408
	s_waitcnt vmcnt(18)
	v_cvt_pk_f16_f32 v224, v224, v225
	v_cvt_pk_f16_f32 v225, v226, v227
	ds_write_b64 v237, v[224:225] offset:21760
	s_waitcnt vmcnt(17)
	v_cvt_pk_f16_f32 v228, v228, v229
	v_cvt_pk_f16_f32 v229, v230, v231
	ds_write_b64 v237, v[228:229] offset:26112
	s_waitcnt vmcnt(16)
	v_cvt_pk_f16_f32 v232, v232, v233
	v_cvt_pk_f16_f32 v233, v234, v235
	ds_write_b64 v237, v[232:233] offset:30464
	global_load_dwordx4 v[204:207], v238, s[40:41] offset:1536 nt
	global_load_dwordx4 v[208:211], v238, s[42:43] offset:1536 nt
	global_load_dwordx4 v[212:215], v238, s[44:45] offset:1536 nt
	global_load_dwordx4 v[216:219], v238, s[46:47] offset:1536 nt
	global_load_dwordx4 v[220:223], v238, s[48:49] offset:1536 nt
	global_load_dwordx4 v[224:227], v238, s[50:51] offset:1536 nt
	global_load_dwordx4 v[228:231], v238, s[52:53] offset:1536 nt
	global_load_dwordx4 v[232:235], v238, s[54:55] offset:1536 nt
	s_waitcnt vmcnt(20)
	s_waitcnt lgkmcnt(11)
	v_mfma_f32_32x32x16_f16 v[82:97], v[130:133], v[146:149], v[82:97]
	v_mfma_f32_32x32x16_f16 v[50:65], v[130:133], v[150:153], v[50:65]
	ds_read_b128 v[130:133], v236 offset:35040
	s_waitcnt lgkmcnt(11)
	v_mfma_f32_32x32x16_f16 v[114:129], v[134:137], v[146:149], v[114:129]
	v_mfma_f32_32x32x16_f16 v[34:49], v[134:137], v[150:153], v[34:49]
	ds_read_b128 v[134:137], v236 offset:39392
	s_waitcnt lgkmcnt(11)
	v_mfma_f32_32x32x16_f16 v[98:113], v[138:141], v[146:149], v[98:113]
	v_mfma_f32_32x32x16_f16 v[18:33], v[138:141], v[150:153], v[18:33]
	ds_read_b128 v[138:141], v236 offset:43744
	s_waitcnt lgkmcnt(11)
	v_mfma_f32_32x32x16_f16 v[66:81], v[142:145], v[146:149], v[66:81]
	v_mfma_f32_32x32x16_f16 v[2:17], v[142:145], v[150:153], v[2:17]
	ds_read_b128 v[142:145], v236 offset:48096
	global_load_dwordx4 v[146:149], v239, s[56:57]
	global_load_dwordx4 v[150:153], v239, s[56:57] offset:512
	s_add_u32 s56, s56, 0x4000
	s_addc_u32 s57, s57, 0
	s_waitcnt vmcnt(20)
	s_waitcnt lgkmcnt(3)
	v_mfma_f32_32x32x16_f16 v[82:97], v[130:133], v[154:157], v[82:97]
	v_mfma_f32_32x32x16_f16 v[50:65], v[130:133], v[158:161], v[50:65]
	s_waitcnt lgkmcnt(2)
	v_mfma_f32_32x32x16_f16 v[114:129], v[134:137], v[154:157], v[114:129]
	v_mfma_f32_32x32x16_f16 v[34:49], v[134:137], v[158:161], v[34:49]
	s_waitcnt lgkmcnt(1)
	v_mfma_f32_32x32x16_f16 v[98:113], v[138:141], v[154:157], v[98:113]
	v_mfma_f32_32x32x16_f16 v[18:33], v[138:141], v[158:161], v[18:33]
	s_waitcnt lgkmcnt(0)
	v_mfma_f32_32x32x16_f16 v[66:81], v[142:145], v[154:157], v[66:81]
	v_mfma_f32_32x32x16_f16 v[2:17], v[142:145], v[158:161], v[2:17]
	global_load_dwordx4 v[154:157], v239, s[56:57]
	global_load_dwordx4 v[158:161], v239, s[56:57] offset:512
	s_add_u32 s56, s56, 0x4000
	s_addc_u32 s57, s57, 0
	s_waitcnt lgkmcnt(0)
	s_barrier
	ds_read_b128 v[130:133], v236
	ds_read_b128 v[134:137], v236 offset:4352
	ds_read_b128 v[138:141], v236 offset:8704
	ds_read_b128 v[142:145], v236 offset:13056
	s_waitcnt vmcnt(20)
	s_waitcnt lgkmcnt(3)
	v_mfma_f32_32x32x16_f16 v[82:97], v[130:133], v[162:165], v[82:97]
	v_mfma_f32_32x32x16_f16 v[50:65], v[130:133], v[166:169], v[50:65]
	ds_read_b128 v[130:133], v236 offset:32
	s_waitcnt lgkmcnt(3)
	v_mfma_f32_32x32x16_f16 v[114:129], v[134:137], v[162:165], v[114:129]
	v_mfma_f32_32x32x16_f16 v[34:49], v[134:137], v[166:169], v[34:49]
	ds_read_b128 v[134:137], v236 offset:4384
	s_waitcnt lgkmcnt(3)
	v_mfma_f32_32x32x16_f16 v[98:113], v[138:141], v[162:165], v[98:113]
	v_mfma_f32_32x32x16_f16 v[18:33], v[138:141], v[166:169], v[18:33]
	ds_read_b128 v[138:141], v236 offset:8736
	s_waitcnt lgkmcnt(3)
	v_mfma_f32_32x32x16_f16 v[66:81], v[142:145], v[162:165], v[66:81]
	v_mfma_f32_32x32x16_f16 v[2:17], v[142:145], v[166:169], v[2:17]
	ds_read_b128 v[142:145], v236 offset:13088
	global_load_dwordx4 v[162:165], v239, s[56:57]
	global_load_dwordx4 v[166:169], v239, s[56:57] offset:512
	s_add_u32 s56, s56, 0x4000
	s_addc_u32 s57, s57, 0
	s_waitcnt vmcnt(20)
	s_waitcnt lgkmcnt(3)
	v_mfma_f32_32x32x16_f16 v[82:97], v[130:133], v[170:173], v[82:97]
	v_mfma_f32_32x32x16_f16 v[50:65], v[130:133], v[174:177], v[50:65]
	ds_read_b128 v[130:133], v236 offset:64
	s_waitcnt lgkmcnt(3)
	v_mfma_f32_32x32x16_f16 v[114:129], v[134:137], v[170:173], v[114:129]
	v_mfma_f32_32x32x16_f16 v[34:49], v[134:137], v[174:177], v[34:49]
	ds_read_b128 v[134:137], v236 offset:4416
	s_waitcnt lgkmcnt(3)
	v_mfma_f32_32x32x16_f16 v[98:113], v[138:141], v[170:173], v[98:113]
	v_mfma_f32_32x32x16_f16 v[18:33], v[138:141], v[174:177], v[18:33]
	ds_read_b128 v[138:141], v236 offset:8768
	s_waitcnt lgkmcnt(3)
	v_mfma_f32_32x32x16_f16 v[66:81], v[142:145], v[170:173], v[66:81]
	v_mfma_f32_32x32x16_f16 v[2:17], v[142:145], v[174:177], v[2:17]
	ds_read_b128 v[142:145], v236 offset:13120
	global_load_dwordx4 v[170:173], v239, s[56:57]
	global_load_dwordx4 v[174:177], v239, s[56:57] offset:512
	s_add_u32 s56, s56, 0x4000
	s_addc_u32 s57, s57, 0
	s_waitcnt vmcnt(20)
	s_waitcnt lgkmcnt(3)
	v_mfma_f32_32x32x16_f16 v[82:97], v[130:133], v[178:181], v[82:97]
	v_mfma_f32_32x32x16_f16 v[50:65], v[130:133], v[182:185], v[50:65]
	ds_read_b128 v[130:133], v236 offset:96
	s_waitcnt lgkmcnt(3)
	v_mfma_f32_32x32x16_f16 v[114:129], v[134:137], v[178:181], v[114:129]
	v_mfma_f32_32x32x16_f16 v[34:49], v[134:137], v[182:185], v[34:49]
	ds_read_b128 v[134:137], v236 offset:4448
	s_waitcnt lgkmcnt(3)
	v_mfma_f32_32x32x16_f16 v[98:113], v[138:141], v[178:181], v[98:113]
	v_mfma_f32_32x32x16_f16 v[18:33], v[138:141], v[182:185], v[18:33]
	ds_read_b128 v[138:141], v236 offset:8800
	s_waitcnt lgkmcnt(3)
	v_mfma_f32_32x32x16_f16 v[66:81], v[142:145], v[178:181], v[66:81]
	v_mfma_f32_32x32x16_f16 v[2:17], v[142:145], v[182:185], v[2:17]
	ds_read_b128 v[142:145], v236 offset:13152
	global_load_dwordx4 v[178:181], v239, s[56:57]
	global_load_dwordx4 v[182:185], v239, s[56:57] offset:512
	s_add_u32 s56, s56, 0x4000
	s_addc_u32 s57, s57, 0
	s_waitcnt vmcnt(20)
	s_waitcnt lgkmcnt(3)
	v_mfma_f32_32x32x16_f16 v[82:97], v[130:133], v[186:189], v[82:97]
	v_mfma_f32_32x32x16_f16 v[50:65], v[130:133], v[190:193], v[50:65]
	ds_read_b128 v[130:133], v236 offset:128
	s_waitcnt lgkmcnt(3)
	v_mfma_f32_32x32x16_f16 v[114:129], v[134:137], v[186:189], v[114:129]
	v_mfma_f32_32x32x16_f16 v[34:49], v[134:137], v[190:193], v[34:49]
	ds_read_b128 v[134:137], v236 offset:4480
	s_waitcnt lgkmcnt(3)
	v_mfma_f32_32x32x16_f16 v[98:113], v[138:141], v[186:189], v[98:113]
	v_mfma_f32_32x32x16_f16 v[18:33], v[138:141], v[190:193], v[18:33]
	ds_read_b128 v[138:141], v236 offset:8832
	s_waitcnt lgkmcnt(3)
	v_mfma_f32_32x32x16_f16 v[66:81], v[142:145], v[186:189], v[66:81]
	v_mfma_f32_32x32x16_f16 v[2:17], v[142:145], v[190:193], v[2:17]
	ds_read_b128 v[142:145], v236 offset:13184
	global_load_dwordx4 v[186:189], v239, s[56:57]
	global_load_dwordx4 v[190:193], v239, s[56:57] offset:512
	s_add_u32 s56, s56, 0x4000
	s_addc_u32 s57, s57, 0
	s_waitcnt vmcnt(20)
	s_waitcnt lgkmcnt(3)
	v_mfma_f32_32x32x16_f16 v[82:97], v[130:133], v[194:197], v[82:97]
	v_mfma_f32_32x32x16_f16 v[50:65], v[130:133], v[198:201], v[50:65]
	ds_read_b128 v[130:133], v236 offset:160
	s_waitcnt lgkmcnt(3)
	v_mfma_f32_32x32x16_f16 v[114:129], v[134:137], v[194:197], v[114:129]
	v_mfma_f32_32x32x16_f16 v[34:49], v[134:137], v[198:201], v[34:49]
	ds_read_b128 v[134:137], v236 offset:4512
	s_waitcnt lgkmcnt(3)
	v_mfma_f32_32x32x16_f16 v[98:113], v[138:141], v[194:197], v[98:113]
	v_mfma_f32_32x32x16_f16 v[18:33], v[138:141], v[198:201], v[18:33]
	ds_read_b128 v[138:141], v236 offset:8864
	s_waitcnt lgkmcnt(3)
	v_mfma_f32_32x32x16_f16 v[66:81], v[142:145], v[194:197], v[66:81]
	v_mfma_f32_32x32x16_f16 v[2:17], v[142:145], v[198:201], v[2:17]
	ds_read_b128 v[142:145], v236 offset:13216
	global_load_dwordx4 v[194:197], v239, s[56:57]
	global_load_dwordx4 v[198:201], v239, s[56:57] offset:512
	s_add_u32 s56, s56, 0x4000
	s_addc_u32 s57, s57, 0
	s_waitcnt vmcnt(12)
	s_waitcnt lgkmcnt(3)
	v_mfma_f32_32x32x16_f16 v[82:97], v[130:133], v[146:149], v[82:97]
	v_mfma_f32_32x32x16_f16 v[50:65], v[130:133], v[150:153], v[50:65]
	ds_read_b128 v[130:133], v236 offset:192
	s_waitcnt lgkmcnt(3)
	v_mfma_f32_32x32x16_f16 v[114:129], v[134:137], v[146:149], v[114:129]
	v_mfma_f32_32x32x16_f16 v[34:49], v[134:137], v[150:153], v[34:49]
	ds_read_b128 v[134:137], v236 offset:4544
	s_waitcnt lgkmcnt(3)
	v_mfma_f32_32x32x16_f16 v[98:113], v[138:141], v[146:149], v[98:113]
	v_mfma_f32_32x32x16_f16 v[18:33], v[138:141], v[150:153], v[18:33]
	ds_read_b128 v[138:141], v236 offset:8896
	s_waitcnt lgkmcnt(3)
	v_mfma_f32_32x32x16_f16 v[66:81], v[142:145], v[146:149], v[66:81]
	v_mfma_f32_32x32x16_f16 v[2:17], v[142:145], v[150:153], v[2:17]
	ds_read_b128 v[142:145], v236 offset:13248
	global_load_dwordx4 v[146:149], v239, s[56:57]
	global_load_dwordx4 v[150:153], v239, s[56:57] offset:512
	s_add_u32 s56, s56, 0x4000
	s_addc_u32 s57, s57, 0
	s_waitcnt vmcnt(23)
	v_cvt_pk_f16_f32 v204, v204, v205
	v_cvt_pk_f16_f32 v205, v206, v207
	ds_write_b64 v237, v[204:205] offset:34816
	s_waitcnt vmcnt(22)
	v_cvt_pk_f16_f32 v208, v208, v209
	v_cvt_pk_f16_f32 v209, v210, v211
	ds_write_b64 v237, v[208:209] offset:39168
	s_waitcnt vmcnt(21)
	v_cvt_pk_f16_f32 v212, v212, v213
	v_cvt_pk_f16_f32 v213, v214, v215
	ds_write_b64 v237, v[212:213] offset:43520
	s_waitcnt vmcnt(20)
	v_cvt_pk_f16_f32 v216, v216, v217
	v_cvt_pk_f16_f32 v217, v218, v219
	ds_write_b64 v237, v[216:217] offset:47872
	s_waitcnt vmcnt(19)
	v_cvt_pk_f16_f32 v220, v220, v221
	v_cvt_pk_f16_f32 v221, v222, v223
	ds_write_b64 v237, v[220:221] offset:52224
	s_waitcnt vmcnt(18)
	v_cvt_pk_f16_f32 v224, v224, v225
	v_cvt_pk_f16_f32 v225, v226, v227
	ds_write_b64 v237, v[224:225] offset:56576
	s_waitcnt vmcnt(17)
	v_cvt_pk_f16_f32 v228, v228, v229
	v_cvt_pk_f16_f32 v229, v230, v231
	ds_write_b64 v237, v[228:229] offset:60928
	s_waitcnt vmcnt(16)
	v_cvt_pk_f16_f32 v232, v232, v233
	v_cvt_pk_f16_f32 v233, v234, v235
	ds_write_b64 v237, v[232:233] offset:65280
	global_load_dwordx4 v[204:207], v238, s[40:41] offset:2048 nt
	global_load_dwordx4 v[208:211], v238, s[42:43] offset:2048 nt
	global_load_dwordx4 v[212:215], v238, s[44:45] offset:2048 nt
	global_load_dwordx4 v[216:219], v238, s[46:47] offset:2048 nt
	global_load_dwordx4 v[220:223], v238, s[48:49] offset:2048 nt
	global_load_dwordx4 v[224:227], v238, s[50:51] offset:2048 nt
	global_load_dwordx4 v[228:231], v238, s[52:53] offset:2048 nt
	global_load_dwordx4 v[232:235], v238, s[54:55] offset:2048 nt
	s_waitcnt vmcnt(20)
	s_waitcnt lgkmcnt(11)
	v_mfma_f32_32x32x16_f16 v[82:97], v[130:133], v[154:157], v[82:97]
	v_mfma_f32_32x32x16_f16 v[50:65], v[130:133], v[158:161], v[50:65]
	ds_read_b128 v[130:133], v236 offset:224
	s_waitcnt lgkmcnt(11)
	v_mfma_f32_32x32x16_f16 v[114:129], v[134:137], v[154:157], v[114:129]
	v_mfma_f32_32x32x16_f16 v[34:49], v[134:137], v[158:161], v[34:49]
	ds_read_b128 v[134:137], v236 offset:4576
	s_waitcnt lgkmcnt(11)
	v_mfma_f32_32x32x16_f16 v[98:113], v[138:141], v[154:157], v[98:113]
	v_mfma_f32_32x32x16_f16 v[18:33], v[138:141], v[158:161], v[18:33]
	ds_read_b128 v[138:141], v236 offset:8928
	s_waitcnt lgkmcnt(11)
	v_mfma_f32_32x32x16_f16 v[66:81], v[142:145], v[154:157], v[66:81]
	v_mfma_f32_32x32x16_f16 v[2:17], v[142:145], v[158:161], v[2:17]
	ds_read_b128 v[142:145], v236 offset:13280
	global_load_dwordx4 v[154:157], v239, s[56:57]
	global_load_dwordx4 v[158:161], v239, s[56:57] offset:512
	s_add_u32 s56, s56, 0x4000
	s_addc_u32 s57, s57, 0
	s_waitcnt vmcnt(20)
	s_waitcnt lgkmcnt(3)
	v_mfma_f32_32x32x16_f16 v[82:97], v[130:133], v[162:165], v[82:97]
	v_mfma_f32_32x32x16_f16 v[50:65], v[130:133], v[166:169], v[50:65]
	s_waitcnt lgkmcnt(2)
	v_mfma_f32_32x32x16_f16 v[114:129], v[134:137], v[162:165], v[114:129]
	v_mfma_f32_32x32x16_f16 v[34:49], v[134:137], v[166:169], v[34:49]
	s_waitcnt lgkmcnt(1)
	v_mfma_f32_32x32x16_f16 v[98:113], v[138:141], v[162:165], v[98:113]
	v_mfma_f32_32x32x16_f16 v[18:33], v[138:141], v[166:169], v[18:33]
	s_waitcnt lgkmcnt(0)
	v_mfma_f32_32x32x16_f16 v[66:81], v[142:145], v[162:165], v[66:81]
	v_mfma_f32_32x32x16_f16 v[2:17], v[142:145], v[166:169], v[2:17]
	global_load_dwordx4 v[162:165], v239, s[56:57]
	global_load_dwordx4 v[166:169], v239, s[56:57] offset:512
	s_add_u32 s56, s56, 0x4000
	s_addc_u32 s57, s57, 0
	s_waitcnt lgkmcnt(0)
	s_barrier
	ds_read_b128 v[130:133], v236 offset:34816
	ds_read_b128 v[134:137], v236 offset:39168
	ds_read_b128 v[138:141], v236 offset:43520
	ds_read_b128 v[142:145], v236 offset:47872
	s_waitcnt vmcnt(20)
	s_waitcnt lgkmcnt(3)
	v_mfma_f32_32x32x16_f16 v[82:97], v[130:133], v[170:173], v[82:97]
	v_mfma_f32_32x32x16_f16 v[50:65], v[130:133], v[174:177], v[50:65]
	ds_read_b128 v[130:133], v236 offset:34848
	s_waitcnt lgkmcnt(3)
	v_mfma_f32_32x32x16_f16 v[114:129], v[134:137], v[170:173], v[114:129]
	v_mfma_f32_32x32x16_f16 v[34:49], v[134:137], v[174:177], v[34:49]
	ds_read_b128 v[134:137], v236 offset:39200
	s_waitcnt lgkmcnt(3)
	v_mfma_f32_32x32x16_f16 v[98:113], v[138:141], v[170:173], v[98:113]
	v_mfma_f32_32x32x16_f16 v[18:33], v[138:141], v[174:177], v[18:33]
	ds_read_b128 v[138:141], v236 offset:43552
	s_waitcnt lgkmcnt(3)
	v_mfma_f32_32x32x16_f16 v[66:81], v[142:145], v[170:173], v[66:81]
	v_mfma_f32_32x32x16_f16 v[2:17], v[142:145], v[174:177], v[2:17]
	ds_read_b128 v[142:145], v236 offset:47904
	global_load_dwordx4 v[170:173], v239, s[56:57]
	global_load_dwordx4 v[174:177], v239, s[56:57] offset:512
	s_add_u32 s56, s56, 0x4000
	s_addc_u32 s57, s57, 0
	s_waitcnt vmcnt(20)
	s_waitcnt lgkmcnt(3)
	v_mfma_f32_32x32x16_f16 v[82:97], v[130:133], v[178:181], v[82:97]
	v_mfma_f32_32x32x16_f16 v[50:65], v[130:133], v[182:185], v[50:65]
	ds_read_b128 v[130:133], v236 offset:34880
	s_waitcnt lgkmcnt(3)
	v_mfma_f32_32x32x16_f16 v[114:129], v[134:137], v[178:181], v[114:129]
	v_mfma_f32_32x32x16_f16 v[34:49], v[134:137], v[182:185], v[34:49]
	ds_read_b128 v[134:137], v236 offset:39232
	s_waitcnt lgkmcnt(3)
	v_mfma_f32_32x32x16_f16 v[98:113], v[138:141], v[178:181], v[98:113]
	v_mfma_f32_32x32x16_f16 v[18:33], v[138:141], v[182:185], v[18:33]
	ds_read_b128 v[138:141], v236 offset:43584
	s_waitcnt lgkmcnt(3)
	v_mfma_f32_32x32x16_f16 v[66:81], v[142:145], v[178:181], v[66:81]
	v_mfma_f32_32x32x16_f16 v[2:17], v[142:145], v[182:185], v[2:17]
	ds_read_b128 v[142:145], v236 offset:47936
	global_load_dwordx4 v[178:181], v239, s[56:57]
	global_load_dwordx4 v[182:185], v239, s[56:57] offset:512
	s_add_u32 s56, s56, 0x4000
	s_addc_u32 s57, s57, 0
	s_waitcnt vmcnt(20)
	s_waitcnt lgkmcnt(3)
	v_mfma_f32_32x32x16_f16 v[82:97], v[130:133], v[186:189], v[82:97]
	v_mfma_f32_32x32x16_f16 v[50:65], v[130:133], v[190:193], v[50:65]
	ds_read_b128 v[130:133], v236 offset:34912
	s_waitcnt lgkmcnt(3)
	v_mfma_f32_32x32x16_f16 v[114:129], v[134:137], v[186:189], v[114:129]
	v_mfma_f32_32x32x16_f16 v[34:49], v[134:137], v[190:193], v[34:49]
	ds_read_b128 v[134:137], v236 offset:39264
	s_waitcnt lgkmcnt(3)
	v_mfma_f32_32x32x16_f16 v[98:113], v[138:141], v[186:189], v[98:113]
	v_mfma_f32_32x32x16_f16 v[18:33], v[138:141], v[190:193], v[18:33]
	ds_read_b128 v[138:141], v236 offset:43616
	s_waitcnt lgkmcnt(3)
	v_mfma_f32_32x32x16_f16 v[66:81], v[142:145], v[186:189], v[66:81]
	v_mfma_f32_32x32x16_f16 v[2:17], v[142:145], v[190:193], v[2:17]
	ds_read_b128 v[142:145], v236 offset:47968
	global_load_dwordx4 v[186:189], v239, s[56:57]
	global_load_dwordx4 v[190:193], v239, s[56:57] offset:512
	s_add_u32 s56, s56, 0x4000
	s_addc_u32 s57, s57, 0
	s_waitcnt vmcnt(20)
	s_waitcnt lgkmcnt(3)
	v_mfma_f32_32x32x16_f16 v[82:97], v[130:133], v[194:197], v[82:97]
	v_mfma_f32_32x32x16_f16 v[50:65], v[130:133], v[198:201], v[50:65]
	ds_read_b128 v[130:133], v236 offset:34944
	s_waitcnt lgkmcnt(3)
	v_mfma_f32_32x32x16_f16 v[114:129], v[134:137], v[194:197], v[114:129]
	v_mfma_f32_32x32x16_f16 v[34:49], v[134:137], v[198:201], v[34:49]
	ds_read_b128 v[134:137], v236 offset:39296
	s_waitcnt lgkmcnt(3)
	v_mfma_f32_32x32x16_f16 v[98:113], v[138:141], v[194:197], v[98:113]
	v_mfma_f32_32x32x16_f16 v[18:33], v[138:141], v[198:201], v[18:33]
	ds_read_b128 v[138:141], v236 offset:43648
	s_waitcnt lgkmcnt(3)
	v_mfma_f32_32x32x16_f16 v[66:81], v[142:145], v[194:197], v[66:81]
	v_mfma_f32_32x32x16_f16 v[2:17], v[142:145], v[198:201], v[2:17]
	ds_read_b128 v[142:145], v236 offset:48000
	global_load_dwordx4 v[194:197], v239, s[56:57]
	global_load_dwordx4 v[198:201], v239, s[56:57] offset:512
	s_add_u32 s56, s56, 0x4000
	s_addc_u32 s57, s57, 0
	s_waitcnt vmcnt(20)
	s_waitcnt lgkmcnt(3)
	v_mfma_f32_32x32x16_f16 v[82:97], v[130:133], v[146:149], v[82:97]
	v_mfma_f32_32x32x16_f16 v[50:65], v[130:133], v[150:153], v[50:65]
	ds_read_b128 v[130:133], v236 offset:34976
	s_waitcnt lgkmcnt(3)
	v_mfma_f32_32x32x16_f16 v[114:129], v[134:137], v[146:149], v[114:129]
	v_mfma_f32_32x32x16_f16 v[34:49], v[134:137], v[150:153], v[34:49]
	ds_read_b128 v[134:137], v236 offset:39328
	s_waitcnt lgkmcnt(3)
	v_mfma_f32_32x32x16_f16 v[98:113], v[138:141], v[146:149], v[98:113]
	v_mfma_f32_32x32x16_f16 v[18:33], v[138:141], v[150:153], v[18:33]
	ds_read_b128 v[138:141], v236 offset:43680
	s_waitcnt lgkmcnt(3)
	v_mfma_f32_32x32x16_f16 v[66:81], v[142:145], v[146:149], v[66:81]
	v_mfma_f32_32x32x16_f16 v[2:17], v[142:145], v[150:153], v[2:17]
	ds_read_b128 v[142:145], v236 offset:48032
	global_load_dwordx4 v[146:149], v239, s[56:57]
	global_load_dwordx4 v[150:153], v239, s[56:57] offset:512
	s_add_u32 s56, s56, 0x4000
	s_addc_u32 s57, s57, 0
	s_waitcnt vmcnt(12)
	s_waitcnt lgkmcnt(3)
	v_mfma_f32_32x32x16_f16 v[82:97], v[130:133], v[154:157], v[82:97]
	v_mfma_f32_32x32x16_f16 v[50:65], v[130:133], v[158:161], v[50:65]
	ds_read_b128 v[130:133], v236 offset:35008
	s_waitcnt lgkmcnt(3)
	v_mfma_f32_32x32x16_f16 v[114:129], v[134:137], v[154:157], v[114:129]
	v_mfma_f32_32x32x16_f16 v[34:49], v[134:137], v[158:161], v[34:49]
	ds_read_b128 v[134:137], v236 offset:39360
	s_waitcnt lgkmcnt(3)
	v_mfma_f32_32x32x16_f16 v[98:113], v[138:141], v[154:157], v[98:113]
	v_mfma_f32_32x32x16_f16 v[18:33], v[138:141], v[158:161], v[18:33]
	ds_read_b128 v[138:141], v236 offset:43712
	s_waitcnt lgkmcnt(3)
	v_mfma_f32_32x32x16_f16 v[66:81], v[142:145], v[154:157], v[66:81]
	v_mfma_f32_32x32x16_f16 v[2:17], v[142:145], v[158:161], v[2:17]
	ds_read_b128 v[142:145], v236 offset:48064
	global_load_dwordx4 v[154:157], v239, s[56:57]
	global_load_dwordx4 v[158:161], v239, s[56:57] offset:512
	s_add_u32 s56, s56, 0x4000
	s_addc_u32 s57, s57, 0
	s_waitcnt vmcnt(23)
	v_cvt_pk_f16_f32 v204, v204, v205
	v_cvt_pk_f16_f32 v205, v206, v207
	ds_write_b64 v237, v[204:205]
	s_waitcnt vmcnt(22)
	v_cvt_pk_f16_f32 v208, v208, v209
	v_cvt_pk_f16_f32 v209, v210, v211
	ds_write_b64 v237, v[208:209] offset:4352
	s_waitcnt vmcnt(21)
	v_cvt_pk_f16_f32 v212, v212, v213
	v_cvt_pk_f16_f32 v213, v214, v215
	ds_write_b64 v237, v[212:213] offset:8704
	s_waitcnt vmcnt(20)
	v_cvt_pk_f16_f32 v216, v216, v217
	v_cvt_pk_f16_f32 v217, v218, v219
	ds_write_b64 v237, v[216:217] offset:13056
	s_waitcnt vmcnt(19)
	v_cvt_pk_f16_f32 v220, v220, v221
	v_cvt_pk_f16_f32 v221, v222, v223
	ds_write_b64 v237, v[220:221] offset:17408
	s_waitcnt vmcnt(18)
	v_cvt_pk_f16_f32 v224, v224, v225
	v_cvt_pk_f16_f32 v225, v226, v227
	ds_write_b64 v237, v[224:225] offset:21760
	s_waitcnt vmcnt(17)
	v_cvt_pk_f16_f32 v228, v228, v229
	v_cvt_pk_f16_f32 v229, v230, v231
	ds_write_b64 v237, v[228:229] offset:26112
	s_waitcnt vmcnt(16)
	v_cvt_pk_f16_f32 v232, v232, v233
	v_cvt_pk_f16_f32 v233, v234, v235
	ds_write_b64 v237, v[232:233] offset:30464
	global_load_dwordx4 v[204:207], v238, s[40:41] offset:2560 nt
	global_load_dwordx4 v[208:211], v238, s[42:43] offset:2560 nt
	global_load_dwordx4 v[212:215], v238, s[44:45] offset:2560 nt
	global_load_dwordx4 v[216:219], v238, s[46:47] offset:2560 nt
	global_load_dwordx4 v[220:223], v238, s[48:49] offset:2560 nt
	global_load_dwordx4 v[224:227], v238, s[50:51] offset:2560 nt
	global_load_dwordx4 v[228:231], v238, s[52:53] offset:2560 nt
	global_load_dwordx4 v[232:235], v238, s[54:55] offset:2560 nt
	s_waitcnt vmcnt(20)
	s_waitcnt lgkmcnt(11)
	v_mfma_f32_32x32x16_f16 v[82:97], v[130:133], v[162:165], v[82:97]
	v_mfma_f32_32x32x16_f16 v[50:65], v[130:133], v[166:169], v[50:65]
	ds_read_b128 v[130:133], v236 offset:35040
	s_waitcnt lgkmcnt(11)
	v_mfma_f32_32x32x16_f16 v[114:129], v[134:137], v[162:165], v[114:129]
	v_mfma_f32_32x32x16_f16 v[34:49], v[134:137], v[166:169], v[34:49]
	ds_read_b128 v[134:137], v236 offset:39392
	s_waitcnt lgkmcnt(11)
	v_mfma_f32_32x32x16_f16 v[98:113], v[138:141], v[162:165], v[98:113]
	v_mfma_f32_32x32x16_f16 v[18:33], v[138:141], v[166:169], v[18:33]
	ds_read_b128 v[138:141], v236 offset:43744
	s_waitcnt lgkmcnt(11)
	v_mfma_f32_32x32x16_f16 v[66:81], v[142:145], v[162:165], v[66:81]
	v_mfma_f32_32x32x16_f16 v[2:17], v[142:145], v[166:169], v[2:17]
	ds_read_b128 v[142:145], v236 offset:48096
	global_load_dwordx4 v[162:165], v239, s[56:57]
	global_load_dwordx4 v[166:169], v239, s[56:57] offset:512
	s_add_u32 s56, s56, 0x4000
	s_addc_u32 s57, s57, 0
	s_waitcnt vmcnt(20)
	s_waitcnt lgkmcnt(3)
	v_mfma_f32_32x32x16_f16 v[82:97], v[130:133], v[170:173], v[82:97]
	v_mfma_f32_32x32x16_f16 v[50:65], v[130:133], v[174:177], v[50:65]
	s_waitcnt lgkmcnt(2)
	v_mfma_f32_32x32x16_f16 v[114:129], v[134:137], v[170:173], v[114:129]
	v_mfma_f32_32x32x16_f16 v[34:49], v[134:137], v[174:177], v[34:49]
	s_waitcnt lgkmcnt(1)
	v_mfma_f32_32x32x16_f16 v[98:113], v[138:141], v[170:173], v[98:113]
	v_mfma_f32_32x32x16_f16 v[18:33], v[138:141], v[174:177], v[18:33]
	s_waitcnt lgkmcnt(0)
	v_mfma_f32_32x32x16_f16 v[66:81], v[142:145], v[170:173], v[66:81]
	v_mfma_f32_32x32x16_f16 v[2:17], v[142:145], v[174:177], v[2:17]
	global_load_dwordx4 v[170:173], v239, s[56:57]
	global_load_dwordx4 v[174:177], v239, s[56:57] offset:512
	s_add_u32 s56, s56, 0x4000
	s_addc_u32 s57, s57, 0
	s_waitcnt lgkmcnt(0)
	s_barrier
	ds_read_b128 v[130:133], v236
	ds_read_b128 v[134:137], v236 offset:4352
	ds_read_b128 v[138:141], v236 offset:8704
	ds_read_b128 v[142:145], v236 offset:13056
	s_waitcnt vmcnt(20)
	s_waitcnt lgkmcnt(3)
	v_mfma_f32_32x32x16_f16 v[82:97], v[130:133], v[178:181], v[82:97]
	v_mfma_f32_32x32x16_f16 v[50:65], v[130:133], v[182:185], v[50:65]
	ds_read_b128 v[130:133], v236 offset:32
	s_waitcnt lgkmcnt(3)
	v_mfma_f32_32x32x16_f16 v[114:129], v[134:137], v[178:181], v[114:129]
	v_mfma_f32_32x32x16_f16 v[34:49], v[134:137], v[182:185], v[34:49]
	ds_read_b128 v[134:137], v236 offset:4384
	s_waitcnt lgkmcnt(3)
	v_mfma_f32_32x32x16_f16 v[98:113], v[138:141], v[178:181], v[98:113]
	v_mfma_f32_32x32x16_f16 v[18:33], v[138:141], v[182:185], v[18:33]
	ds_read_b128 v[138:141], v236 offset:8736
	s_waitcnt lgkmcnt(3)
	v_mfma_f32_32x32x16_f16 v[66:81], v[142:145], v[178:181], v[66:81]
	v_mfma_f32_32x32x16_f16 v[2:17], v[142:145], v[182:185], v[2:17]
	ds_read_b128 v[142:145], v236 offset:13088
	global_load_dwordx4 v[178:181], v239, s[56:57]
	global_load_dwordx4 v[182:185], v239, s[56:57] offset:512
	s_add_u32 s56, s56, 0x4000
	s_addc_u32 s57, s57, 0
	s_waitcnt vmcnt(20)
	s_waitcnt lgkmcnt(3)
	v_mfma_f32_32x32x16_f16 v[82:97], v[130:133], v[186:189], v[82:97]
	v_mfma_f32_32x32x16_f16 v[50:65], v[130:133], v[190:193], v[50:65]
	ds_read_b128 v[130:133], v236 offset:64
	s_waitcnt lgkmcnt(3)
	v_mfma_f32_32x32x16_f16 v[114:129], v[134:137], v[186:189], v[114:129]
	v_mfma_f32_32x32x16_f16 v[34:49], v[134:137], v[190:193], v[34:49]
	ds_read_b128 v[134:137], v236 offset:4416
	s_waitcnt lgkmcnt(3)
	v_mfma_f32_32x32x16_f16 v[98:113], v[138:141], v[186:189], v[98:113]
	v_mfma_f32_32x32x16_f16 v[18:33], v[138:141], v[190:193], v[18:33]
	ds_read_b128 v[138:141], v236 offset:8768
	s_waitcnt lgkmcnt(3)
	v_mfma_f32_32x32x16_f16 v[66:81], v[142:145], v[186:189], v[66:81]
	v_mfma_f32_32x32x16_f16 v[2:17], v[142:145], v[190:193], v[2:17]
	ds_read_b128 v[142:145], v236 offset:13120
	global_load_dwordx4 v[186:189], v239, s[56:57]
	global_load_dwordx4 v[190:193], v239, s[56:57] offset:512
	s_add_u32 s56, s56, 0x4000
	s_addc_u32 s57, s57, 0
	s_waitcnt vmcnt(20)
	s_waitcnt lgkmcnt(3)
	v_mfma_f32_32x32x16_f16 v[82:97], v[130:133], v[194:197], v[82:97]
	v_mfma_f32_32x32x16_f16 v[50:65], v[130:133], v[198:201], v[50:65]
	ds_read_b128 v[130:133], v236 offset:96
	s_waitcnt lgkmcnt(3)
	v_mfma_f32_32x32x16_f16 v[114:129], v[134:137], v[194:197], v[114:129]
	v_mfma_f32_32x32x16_f16 v[34:49], v[134:137], v[198:201], v[34:49]
	ds_read_b128 v[134:137], v236 offset:4448
	s_waitcnt lgkmcnt(3)
	v_mfma_f32_32x32x16_f16 v[98:113], v[138:141], v[194:197], v[98:113]
	v_mfma_f32_32x32x16_f16 v[18:33], v[138:141], v[198:201], v[18:33]
	ds_read_b128 v[138:141], v236 offset:8800
	s_waitcnt lgkmcnt(3)
	v_mfma_f32_32x32x16_f16 v[66:81], v[142:145], v[194:197], v[66:81]
	v_mfma_f32_32x32x16_f16 v[2:17], v[142:145], v[198:201], v[2:17]
	ds_read_b128 v[142:145], v236 offset:13152
	global_load_dwordx4 v[194:197], v239, s[56:57]
	global_load_dwordx4 v[198:201], v239, s[56:57] offset:512
	s_add_u32 s56, s56, 0x4000
	s_addc_u32 s57, s57, 0
	s_waitcnt vmcnt(20)
	s_waitcnt lgkmcnt(3)
	v_mfma_f32_32x32x16_f16 v[82:97], v[130:133], v[146:149], v[82:97]
	v_mfma_f32_32x32x16_f16 v[50:65], v[130:133], v[150:153], v[50:65]
	ds_read_b128 v[130:133], v236 offset:128
	s_waitcnt lgkmcnt(3)
	v_mfma_f32_32x32x16_f16 v[114:129], v[134:137], v[146:149], v[114:129]
	v_mfma_f32_32x32x16_f16 v[34:49], v[134:137], v[150:153], v[34:49]
	ds_read_b128 v[134:137], v236 offset:4480
	s_waitcnt lgkmcnt(3)
	v_mfma_f32_32x32x16_f16 v[98:113], v[138:141], v[146:149], v[98:113]
	v_mfma_f32_32x32x16_f16 v[18:33], v[138:141], v[150:153], v[18:33]
	ds_read_b128 v[138:141], v236 offset:8832
	s_waitcnt lgkmcnt(3)
	v_mfma_f32_32x32x16_f16 v[66:81], v[142:145], v[146:149], v[66:81]
	v_mfma_f32_32x32x16_f16 v[2:17], v[142:145], v[150:153], v[2:17]
	ds_read_b128 v[142:145], v236 offset:13184
	global_load_dwordx4 v[146:149], v239, s[56:57]
	global_load_dwordx4 v[150:153], v239, s[56:57] offset:512
	s_add_u32 s56, s56, 0x4000
	s_addc_u32 s57, s57, 0
	s_waitcnt vmcnt(20)
	s_waitcnt lgkmcnt(3)
	v_mfma_f32_32x32x16_f16 v[82:97], v[130:133], v[154:157], v[82:97]
	v_mfma_f32_32x32x16_f16 v[50:65], v[130:133], v[158:161], v[50:65]
	ds_read_b128 v[130:133], v236 offset:160
	s_waitcnt lgkmcnt(3)
	v_mfma_f32_32x32x16_f16 v[114:129], v[134:137], v[154:157], v[114:129]
	v_mfma_f32_32x32x16_f16 v[34:49], v[134:137], v[158:161], v[34:49]
	ds_read_b128 v[134:137], v236 offset:4512
	s_waitcnt lgkmcnt(3)
	v_mfma_f32_32x32x16_f16 v[98:113], v[138:141], v[154:157], v[98:113]
	v_mfma_f32_32x32x16_f16 v[18:33], v[138:141], v[158:161], v[18:33]
	ds_read_b128 v[138:141], v236 offset:8864
	s_waitcnt lgkmcnt(3)
	v_mfma_f32_32x32x16_f16 v[66:81], v[142:145], v[154:157], v[66:81]
	v_mfma_f32_32x32x16_f16 v[2:17], v[142:145], v[158:161], v[2:17]
	ds_read_b128 v[142:145], v236 offset:13216
	global_load_dwordx4 v[154:157], v239, s[56:57]
	global_load_dwordx4 v[158:161], v239, s[56:57] offset:512
	s_add_u32 s56, s56, 0x4000
	s_addc_u32 s57, s57, 0
	s_waitcnt vmcnt(12)
	s_waitcnt lgkmcnt(3)
	v_mfma_f32_32x32x16_f16 v[82:97], v[130:133], v[162:165], v[82:97]
	v_mfma_f32_32x32x16_f16 v[50:65], v[130:133], v[166:169], v[50:65]
	ds_read_b128 v[130:133], v236 offset:192
	s_waitcnt lgkmcnt(3)
	v_mfma_f32_32x32x16_f16 v[114:129], v[134:137], v[162:165], v[114:129]
	v_mfma_f32_32x32x16_f16 v[34:49], v[134:137], v[166:169], v[34:49]
	ds_read_b128 v[134:137], v236 offset:4544
	s_waitcnt lgkmcnt(3)
	v_mfma_f32_32x32x16_f16 v[98:113], v[138:141], v[162:165], v[98:113]
	v_mfma_f32_32x32x16_f16 v[18:33], v[138:141], v[166:169], v[18:33]
	ds_read_b128 v[138:141], v236 offset:8896
	s_waitcnt lgkmcnt(3)
	v_mfma_f32_32x32x16_f16 v[66:81], v[142:145], v[162:165], v[66:81]
	v_mfma_f32_32x32x16_f16 v[2:17], v[142:145], v[166:169], v[2:17]
	ds_read_b128 v[142:145], v236 offset:13248
	global_load_dwordx4 v[162:165], v239, s[56:57]
	global_load_dwordx4 v[166:169], v239, s[56:57] offset:512
	s_add_u32 s56, s56, 0x4000
	s_addc_u32 s57, s57, 0
	s_waitcnt vmcnt(23)
	v_cvt_pk_f16_f32 v204, v204, v205
	v_cvt_pk_f16_f32 v205, v206, v207
	ds_write_b64 v237, v[204:205] offset:34816
	s_waitcnt vmcnt(22)
	v_cvt_pk_f16_f32 v208, v208, v209
	v_cvt_pk_f16_f32 v209, v210, v211
	ds_write_b64 v237, v[208:209] offset:39168
	s_waitcnt vmcnt(21)
	v_cvt_pk_f16_f32 v212, v212, v213
	v_cvt_pk_f16_f32 v213, v214, v215
	ds_write_b64 v237, v[212:213] offset:43520
	s_waitcnt vmcnt(20)
	v_cvt_pk_f16_f32 v216, v216, v217
	v_cvt_pk_f16_f32 v217, v218, v219
	ds_write_b64 v237, v[216:217] offset:47872
	s_waitcnt vmcnt(19)
	v_cvt_pk_f16_f32 v220, v220, v221
	v_cvt_pk_f16_f32 v221, v222, v223
	ds_write_b64 v237, v[220:221] offset:52224
	s_waitcnt vmcnt(18)
	v_cvt_pk_f16_f32 v224, v224, v225
	v_cvt_pk_f16_f32 v225, v226, v227
	ds_write_b64 v237, v[224:225] offset:56576
	s_waitcnt vmcnt(17)
	v_cvt_pk_f16_f32 v228, v228, v229
	v_cvt_pk_f16_f32 v229, v230, v231
	ds_write_b64 v237, v[228:229] offset:60928
	s_waitcnt vmcnt(16)
	v_cvt_pk_f16_f32 v232, v232, v233
	v_cvt_pk_f16_f32 v233, v234, v235
	ds_write_b64 v237, v[232:233] offset:65280
	global_load_dwordx4 v[204:207], v238, s[40:41] offset:3072 nt
	global_load_dwordx4 v[208:211], v238, s[42:43] offset:3072 nt
	global_load_dwordx4 v[212:215], v238, s[44:45] offset:3072 nt
	global_load_dwordx4 v[216:219], v238, s[46:47] offset:3072 nt
	global_load_dwordx4 v[220:223], v238, s[48:49] offset:3072 nt
	global_load_dwordx4 v[224:227], v238, s[50:51] offset:3072 nt
	global_load_dwordx4 v[228:231], v238, s[52:53] offset:3072 nt
	global_load_dwordx4 v[232:235], v238, s[54:55] offset:3072 nt
	s_waitcnt vmcnt(20)
	s_waitcnt lgkmcnt(11)
	v_mfma_f32_32x32x16_f16 v[82:97], v[130:133], v[170:173], v[82:97]
	v_mfma_f32_32x32x16_f16 v[50:65], v[130:133], v[174:177], v[50:65]
	ds_read_b128 v[130:133], v236 offset:224
	s_waitcnt lgkmcnt(11)
	v_mfma_f32_32x32x16_f16 v[114:129], v[134:137], v[170:173], v[114:129]
	v_mfma_f32_32x32x16_f16 v[34:49], v[134:137], v[174:177], v[34:49]
	ds_read_b128 v[134:137], v236 offset:4576
	s_waitcnt lgkmcnt(11)
	v_mfma_f32_32x32x16_f16 v[98:113], v[138:141], v[170:173], v[98:113]
	v_mfma_f32_32x32x16_f16 v[18:33], v[138:141], v[174:177], v[18:33]
	ds_read_b128 v[138:141], v236 offset:8928
	s_waitcnt lgkmcnt(11)
	v_mfma_f32_32x32x16_f16 v[66:81], v[142:145], v[170:173], v[66:81]
	v_mfma_f32_32x32x16_f16 v[2:17], v[142:145], v[174:177], v[2:17]
	ds_read_b128 v[142:145], v236 offset:13280
	global_load_dwordx4 v[170:173], v239, s[56:57]
	global_load_dwordx4 v[174:177], v239, s[56:57] offset:512
	s_add_u32 s56, s56, 0x4000
	s_addc_u32 s57, s57, 0
	s_waitcnt vmcnt(20)
	s_waitcnt lgkmcnt(3)
	v_mfma_f32_32x32x16_f16 v[82:97], v[130:133], v[178:181], v[82:97]
	v_mfma_f32_32x32x16_f16 v[50:65], v[130:133], v[182:185], v[50:65]
	s_waitcnt lgkmcnt(2)
	v_mfma_f32_32x32x16_f16 v[114:129], v[134:137], v[178:181], v[114:129]
	v_mfma_f32_32x32x16_f16 v[34:49], v[134:137], v[182:185], v[34:49]
	s_waitcnt lgkmcnt(1)
	v_mfma_f32_32x32x16_f16 v[98:113], v[138:141], v[178:181], v[98:113]
	v_mfma_f32_32x32x16_f16 v[18:33], v[138:141], v[182:185], v[18:33]
	s_waitcnt lgkmcnt(0)
	v_mfma_f32_32x32x16_f16 v[66:81], v[142:145], v[178:181], v[66:81]
	v_mfma_f32_32x32x16_f16 v[2:17], v[142:145], v[182:185], v[2:17]
	global_load_dwordx4 v[178:181], v239, s[56:57]
	global_load_dwordx4 v[182:185], v239, s[56:57] offset:512
	s_add_u32 s56, s56, 0x4000
	s_addc_u32 s57, s57, 0
	s_waitcnt lgkmcnt(0)
	s_barrier
	ds_read_b128 v[130:133], v236 offset:34816
	ds_read_b128 v[134:137], v236 offset:39168
	ds_read_b128 v[138:141], v236 offset:43520
	ds_read_b128 v[142:145], v236 offset:47872
	s_waitcnt vmcnt(20)
	s_waitcnt lgkmcnt(3)
	v_mfma_f32_32x32x16_f16 v[82:97], v[130:133], v[186:189], v[82:97]
	v_mfma_f32_32x32x16_f16 v[50:65], v[130:133], v[190:193], v[50:65]
	ds_read_b128 v[130:133], v236 offset:34848
	s_waitcnt lgkmcnt(3)
	v_mfma_f32_32x32x16_f16 v[114:129], v[134:137], v[186:189], v[114:129]
	v_mfma_f32_32x32x16_f16 v[34:49], v[134:137], v[190:193], v[34:49]
	ds_read_b128 v[134:137], v236 offset:39200
	s_waitcnt lgkmcnt(3)
	v_mfma_f32_32x32x16_f16 v[98:113], v[138:141], v[186:189], v[98:113]
	v_mfma_f32_32x32x16_f16 v[18:33], v[138:141], v[190:193], v[18:33]
	ds_read_b128 v[138:141], v236 offset:43552
	s_waitcnt lgkmcnt(3)
	v_mfma_f32_32x32x16_f16 v[66:81], v[142:145], v[186:189], v[66:81]
	v_mfma_f32_32x32x16_f16 v[2:17], v[142:145], v[190:193], v[2:17]
	ds_read_b128 v[142:145], v236 offset:47904
	global_load_dwordx4 v[186:189], v239, s[56:57]
	global_load_dwordx4 v[190:193], v239, s[56:57] offset:512
	s_add_u32 s56, s56, 0x4000
	s_addc_u32 s57, s57, 0
	s_waitcnt vmcnt(20)
	s_waitcnt lgkmcnt(3)
	v_mfma_f32_32x32x16_f16 v[82:97], v[130:133], v[194:197], v[82:97]
	v_mfma_f32_32x32x16_f16 v[50:65], v[130:133], v[198:201], v[50:65]
	ds_read_b128 v[130:133], v236 offset:34880
	s_waitcnt lgkmcnt(3)
	v_mfma_f32_32x32x16_f16 v[114:129], v[134:137], v[194:197], v[114:129]
	v_mfma_f32_32x32x16_f16 v[34:49], v[134:137], v[198:201], v[34:49]
	ds_read_b128 v[134:137], v236 offset:39232
	s_waitcnt lgkmcnt(3)
	v_mfma_f32_32x32x16_f16 v[98:113], v[138:141], v[194:197], v[98:113]
	v_mfma_f32_32x32x16_f16 v[18:33], v[138:141], v[198:201], v[18:33]
	ds_read_b128 v[138:141], v236 offset:43584
	s_waitcnt lgkmcnt(3)
	v_mfma_f32_32x32x16_f16 v[66:81], v[142:145], v[194:197], v[66:81]
	v_mfma_f32_32x32x16_f16 v[2:17], v[142:145], v[198:201], v[2:17]
	ds_read_b128 v[142:145], v236 offset:47936
	global_load_dwordx4 v[194:197], v239, s[56:57]
	global_load_dwordx4 v[198:201], v239, s[56:57] offset:512
	s_add_u32 s56, s56, 0x4000
	s_addc_u32 s57, s57, 0
	s_waitcnt vmcnt(20)
	s_waitcnt lgkmcnt(3)
	v_mfma_f32_32x32x16_f16 v[82:97], v[130:133], v[146:149], v[82:97]
	v_mfma_f32_32x32x16_f16 v[50:65], v[130:133], v[150:153], v[50:65]
	ds_read_b128 v[130:133], v236 offset:34912
	s_waitcnt lgkmcnt(3)
	v_mfma_f32_32x32x16_f16 v[114:129], v[134:137], v[146:149], v[114:129]
	v_mfma_f32_32x32x16_f16 v[34:49], v[134:137], v[150:153], v[34:49]
	ds_read_b128 v[134:137], v236 offset:39264
	s_waitcnt lgkmcnt(3)
	v_mfma_f32_32x32x16_f16 v[98:113], v[138:141], v[146:149], v[98:113]
	v_mfma_f32_32x32x16_f16 v[18:33], v[138:141], v[150:153], v[18:33]
	ds_read_b128 v[138:141], v236 offset:43616
	s_waitcnt lgkmcnt(3)
	v_mfma_f32_32x32x16_f16 v[66:81], v[142:145], v[146:149], v[66:81]
	v_mfma_f32_32x32x16_f16 v[2:17], v[142:145], v[150:153], v[2:17]
	ds_read_b128 v[142:145], v236 offset:47968
	global_load_dwordx4 v[146:149], v239, s[56:57]
	global_load_dwordx4 v[150:153], v239, s[56:57] offset:512
	s_add_u32 s56, s56, 0x4000
	s_addc_u32 s57, s57, 0
	s_waitcnt vmcnt(20)
	s_waitcnt lgkmcnt(3)
	v_mfma_f32_32x32x16_f16 v[82:97], v[130:133], v[154:157], v[82:97]
	v_mfma_f32_32x32x16_f16 v[50:65], v[130:133], v[158:161], v[50:65]
	ds_read_b128 v[130:133], v236 offset:34944
	s_waitcnt lgkmcnt(3)
	v_mfma_f32_32x32x16_f16 v[114:129], v[134:137], v[154:157], v[114:129]
	v_mfma_f32_32x32x16_f16 v[34:49], v[134:137], v[158:161], v[34:49]
	ds_read_b128 v[134:137], v236 offset:39296
	s_waitcnt lgkmcnt(3)
	v_mfma_f32_32x32x16_f16 v[98:113], v[138:141], v[154:157], v[98:113]
	v_mfma_f32_32x32x16_f16 v[18:33], v[138:141], v[158:161], v[18:33]
	ds_read_b128 v[138:141], v236 offset:43648
	s_waitcnt lgkmcnt(3)
	v_mfma_f32_32x32x16_f16 v[66:81], v[142:145], v[154:157], v[66:81]
	v_mfma_f32_32x32x16_f16 v[2:17], v[142:145], v[158:161], v[2:17]
	ds_read_b128 v[142:145], v236 offset:48000
	global_load_dwordx4 v[154:157], v239, s[56:57]
	global_load_dwordx4 v[158:161], v239, s[56:57] offset:512
	s_add_u32 s56, s56, 0x4000
	s_addc_u32 s57, s57, 0
	s_waitcnt vmcnt(20)
	s_waitcnt lgkmcnt(3)
	v_mfma_f32_32x32x16_f16 v[82:97], v[130:133], v[162:165], v[82:97]
	v_mfma_f32_32x32x16_f16 v[50:65], v[130:133], v[166:169], v[50:65]
	ds_read_b128 v[130:133], v236 offset:34976
	s_waitcnt lgkmcnt(3)
	v_mfma_f32_32x32x16_f16 v[114:129], v[134:137], v[162:165], v[114:129]
	v_mfma_f32_32x32x16_f16 v[34:49], v[134:137], v[166:169], v[34:49]
	ds_read_b128 v[134:137], v236 offset:39328
	s_waitcnt lgkmcnt(3)
	v_mfma_f32_32x32x16_f16 v[98:113], v[138:141], v[162:165], v[98:113]
	v_mfma_f32_32x32x16_f16 v[18:33], v[138:141], v[166:169], v[18:33]
	ds_read_b128 v[138:141], v236 offset:43680
	s_waitcnt lgkmcnt(3)
	v_mfma_f32_32x32x16_f16 v[66:81], v[142:145], v[162:165], v[66:81]
	v_mfma_f32_32x32x16_f16 v[2:17], v[142:145], v[166:169], v[2:17]
	ds_read_b128 v[142:145], v236 offset:48032
	global_load_dwordx4 v[162:165], v239, s[56:57]
	global_load_dwordx4 v[166:169], v239, s[56:57] offset:512
	s_add_u32 s56, s56, 0x4000
	s_addc_u32 s57, s57, 0
	s_waitcnt vmcnt(12)
	s_waitcnt lgkmcnt(3)
	v_mfma_f32_32x32x16_f16 v[82:97], v[130:133], v[170:173], v[82:97]
	v_mfma_f32_32x32x16_f16 v[50:65], v[130:133], v[174:177], v[50:65]
	ds_read_b128 v[130:133], v236 offset:35008
	s_waitcnt lgkmcnt(3)
	v_mfma_f32_32x32x16_f16 v[114:129], v[134:137], v[170:173], v[114:129]
	v_mfma_f32_32x32x16_f16 v[34:49], v[134:137], v[174:177], v[34:49]
	ds_read_b128 v[134:137], v236 offset:39360
	s_waitcnt lgkmcnt(3)
	v_mfma_f32_32x32x16_f16 v[98:113], v[138:141], v[170:173], v[98:113]
	v_mfma_f32_32x32x16_f16 v[18:33], v[138:141], v[174:177], v[18:33]
	ds_read_b128 v[138:141], v236 offset:43712
	s_waitcnt lgkmcnt(3)
	v_mfma_f32_32x32x16_f16 v[66:81], v[142:145], v[170:173], v[66:81]
	v_mfma_f32_32x32x16_f16 v[2:17], v[142:145], v[174:177], v[2:17]
	ds_read_b128 v[142:145], v236 offset:48064
	global_load_dwordx4 v[170:173], v239, s[56:57]
	global_load_dwordx4 v[174:177], v239, s[56:57] offset:512
	s_add_u32 s56, s56, 0x4000
	s_addc_u32 s57, s57, 0
	s_waitcnt vmcnt(23)
	v_cvt_pk_f16_f32 v204, v204, v205
	v_cvt_pk_f16_f32 v205, v206, v207
	ds_write_b64 v237, v[204:205]
	s_waitcnt vmcnt(22)
	v_cvt_pk_f16_f32 v208, v208, v209
	v_cvt_pk_f16_f32 v209, v210, v211
	ds_write_b64 v237, v[208:209] offset:4352
	s_waitcnt vmcnt(21)
	v_cvt_pk_f16_f32 v212, v212, v213
	v_cvt_pk_f16_f32 v213, v214, v215
	ds_write_b64 v237, v[212:213] offset:8704
	s_waitcnt vmcnt(20)
	v_cvt_pk_f16_f32 v216, v216, v217
	v_cvt_pk_f16_f32 v217, v218, v219
	ds_write_b64 v237, v[216:217] offset:13056
	s_waitcnt vmcnt(19)
	v_cvt_pk_f16_f32 v220, v220, v221
	v_cvt_pk_f16_f32 v221, v222, v223
	ds_write_b64 v237, v[220:221] offset:17408
	s_waitcnt vmcnt(18)
	v_cvt_pk_f16_f32 v224, v224, v225
	v_cvt_pk_f16_f32 v225, v226, v227
	ds_write_b64 v237, v[224:225] offset:21760
	s_waitcnt vmcnt(17)
	v_cvt_pk_f16_f32 v228, v228, v229
	v_cvt_pk_f16_f32 v229, v230, v231
	ds_write_b64 v237, v[228:229] offset:26112
	s_waitcnt vmcnt(16)
	v_cvt_pk_f16_f32 v232, v232, v233
	v_cvt_pk_f16_f32 v233, v234, v235
	ds_write_b64 v237, v[232:233] offset:30464
	global_load_dwordx4 v[204:207], v238, s[40:41] offset:3584 nt
	global_load_dwordx4 v[208:211], v238, s[42:43] offset:3584 nt
	global_load_dwordx4 v[212:215], v238, s[44:45] offset:3584 nt
	global_load_dwordx4 v[216:219], v238, s[46:47] offset:3584 nt
	global_load_dwordx4 v[220:223], v238, s[48:49] offset:3584 nt
	global_load_dwordx4 v[224:227], v238, s[50:51] offset:3584 nt
	global_load_dwordx4 v[228:231], v238, s[52:53] offset:3584 nt
	global_load_dwordx4 v[232:235], v238, s[54:55] offset:3584 nt
	s_waitcnt vmcnt(20)
	s_waitcnt lgkmcnt(11)
	v_mfma_f32_32x32x16_f16 v[82:97], v[130:133], v[178:181], v[82:97]
	v_mfma_f32_32x32x16_f16 v[50:65], v[130:133], v[182:185], v[50:65]
	ds_read_b128 v[130:133], v236 offset:35040
	s_waitcnt lgkmcnt(11)
	v_mfma_f32_32x32x16_f16 v[114:129], v[134:137], v[178:181], v[114:129]
	v_mfma_f32_32x32x16_f16 v[34:49], v[134:137], v[182:185], v[34:49]
	ds_read_b128 v[134:137], v236 offset:39392
	s_waitcnt lgkmcnt(11)
	v_mfma_f32_32x32x16_f16 v[98:113], v[138:141], v[178:181], v[98:113]
	v_mfma_f32_32x32x16_f16 v[18:33], v[138:141], v[182:185], v[18:33]
	ds_read_b128 v[138:141], v236 offset:43744
	s_waitcnt lgkmcnt(11)
	v_mfma_f32_32x32x16_f16 v[66:81], v[142:145], v[178:181], v[66:81]
	v_mfma_f32_32x32x16_f16 v[2:17], v[142:145], v[182:185], v[2:17]
	ds_read_b128 v[142:145], v236 offset:48096
	global_load_dwordx4 v[178:181], v239, s[56:57]
	global_load_dwordx4 v[182:185], v239, s[56:57] offset:512
	s_add_u32 s56, s56, 0x4000
	s_addc_u32 s57, s57, 0
	s_waitcnt vmcnt(20)
	s_waitcnt lgkmcnt(3)
	v_mfma_f32_32x32x16_f16 v[82:97], v[130:133], v[186:189], v[82:97]
	v_mfma_f32_32x32x16_f16 v[50:65], v[130:133], v[190:193], v[50:65]
	s_waitcnt lgkmcnt(2)
	v_mfma_f32_32x32x16_f16 v[114:129], v[134:137], v[186:189], v[114:129]
	v_mfma_f32_32x32x16_f16 v[34:49], v[134:137], v[190:193], v[34:49]
	s_waitcnt lgkmcnt(1)
	v_mfma_f32_32x32x16_f16 v[98:113], v[138:141], v[186:189], v[98:113]
	v_mfma_f32_32x32x16_f16 v[18:33], v[138:141], v[190:193], v[18:33]
	s_waitcnt lgkmcnt(0)
	v_mfma_f32_32x32x16_f16 v[66:81], v[142:145], v[186:189], v[66:81]
	v_mfma_f32_32x32x16_f16 v[2:17], v[142:145], v[190:193], v[2:17]
	global_load_dwordx4 v[186:189], v239, s[56:57]
	global_load_dwordx4 v[190:193], v239, s[56:57] offset:512
	s_add_u32 s56, s56, 0x4000
	s_addc_u32 s57, s57, 0
	s_waitcnt lgkmcnt(0)
	s_barrier
	ds_read_b128 v[130:133], v236
	ds_read_b128 v[134:137], v236 offset:4352
	ds_read_b128 v[138:141], v236 offset:8704
	ds_read_b128 v[142:145], v236 offset:13056
	s_waitcnt vmcnt(20)
	s_waitcnt lgkmcnt(3)
	v_mfma_f32_32x32x16_f16 v[82:97], v[130:133], v[194:197], v[82:97]
	v_mfma_f32_32x32x16_f16 v[50:65], v[130:133], v[198:201], v[50:65]
	ds_read_b128 v[130:133], v236 offset:32
	s_waitcnt lgkmcnt(3)
	v_mfma_f32_32x32x16_f16 v[114:129], v[134:137], v[194:197], v[114:129]
	v_mfma_f32_32x32x16_f16 v[34:49], v[134:137], v[198:201], v[34:49]
	ds_read_b128 v[134:137], v236 offset:4384
	s_waitcnt lgkmcnt(3)
	v_mfma_f32_32x32x16_f16 v[98:113], v[138:141], v[194:197], v[98:113]
	v_mfma_f32_32x32x16_f16 v[18:33], v[138:141], v[198:201], v[18:33]
	ds_read_b128 v[138:141], v236 offset:8736
	s_waitcnt lgkmcnt(3)
	v_mfma_f32_32x32x16_f16 v[66:81], v[142:145], v[194:197], v[66:81]
	v_mfma_f32_32x32x16_f16 v[2:17], v[142:145], v[198:201], v[2:17]
	ds_read_b128 v[142:145], v236 offset:13088
	global_load_dwordx4 v[194:197], v239, s[56:57]
	global_load_dwordx4 v[198:201], v239, s[56:57] offset:512
	s_add_u32 s56, s56, 0x4000
	s_addc_u32 s57, s57, 0
	s_waitcnt vmcnt(20)
	s_waitcnt lgkmcnt(3)
	v_mfma_f32_32x32x16_f16 v[82:97], v[130:133], v[146:149], v[82:97]
	v_mfma_f32_32x32x16_f16 v[50:65], v[130:133], v[150:153], v[50:65]
	ds_read_b128 v[130:133], v236 offset:64
	s_waitcnt lgkmcnt(3)
	v_mfma_f32_32x32x16_f16 v[114:129], v[134:137], v[146:149], v[114:129]
	v_mfma_f32_32x32x16_f16 v[34:49], v[134:137], v[150:153], v[34:49]
	ds_read_b128 v[134:137], v236 offset:4416
	s_waitcnt lgkmcnt(3)
	v_mfma_f32_32x32x16_f16 v[98:113], v[138:141], v[146:149], v[98:113]
	v_mfma_f32_32x32x16_f16 v[18:33], v[138:141], v[150:153], v[18:33]
	ds_read_b128 v[138:141], v236 offset:8768
	s_waitcnt lgkmcnt(3)
	v_mfma_f32_32x32x16_f16 v[66:81], v[142:145], v[146:149], v[66:81]
	v_mfma_f32_32x32x16_f16 v[2:17], v[142:145], v[150:153], v[2:17]
	ds_read_b128 v[142:145], v236 offset:13120
	global_load_dwordx4 v[146:149], v239, s[56:57]
	global_load_dwordx4 v[150:153], v239, s[56:57] offset:512
	s_add_u32 s56, s56, 0x4000
	s_addc_u32 s57, s57, 0
	s_waitcnt vmcnt(20)
	s_waitcnt lgkmcnt(3)
	v_mfma_f32_32x32x16_f16 v[82:97], v[130:133], v[154:157], v[82:97]
	v_mfma_f32_32x32x16_f16 v[50:65], v[130:133], v[158:161], v[50:65]
	ds_read_b128 v[130:133], v236 offset:96
	s_waitcnt lgkmcnt(3)
	v_mfma_f32_32x32x16_f16 v[114:129], v[134:137], v[154:157], v[114:129]
	v_mfma_f32_32x32x16_f16 v[34:49], v[134:137], v[158:161], v[34:49]
	ds_read_b128 v[134:137], v236 offset:4448
	s_waitcnt lgkmcnt(3)
	v_mfma_f32_32x32x16_f16 v[98:113], v[138:141], v[154:157], v[98:113]
	v_mfma_f32_32x32x16_f16 v[18:33], v[138:141], v[158:161], v[18:33]
	ds_read_b128 v[138:141], v236 offset:8800
	s_waitcnt lgkmcnt(3)
	v_mfma_f32_32x32x16_f16 v[66:81], v[142:145], v[154:157], v[66:81]
	v_mfma_f32_32x32x16_f16 v[2:17], v[142:145], v[158:161], v[2:17]
	ds_read_b128 v[142:145], v236 offset:13152
	global_load_dwordx4 v[154:157], v239, s[56:57]
	global_load_dwordx4 v[158:161], v239, s[56:57] offset:512
	s_add_u32 s56, s56, 0x4000
	s_addc_u32 s57, s57, 0
	s_waitcnt vmcnt(20)
	s_waitcnt lgkmcnt(3)
	v_mfma_f32_32x32x16_f16 v[82:97], v[130:133], v[162:165], v[82:97]
	v_mfma_f32_32x32x16_f16 v[50:65], v[130:133], v[166:169], v[50:65]
	ds_read_b128 v[130:133], v236 offset:128
	s_waitcnt lgkmcnt(3)
	v_mfma_f32_32x32x16_f16 v[114:129], v[134:137], v[162:165], v[114:129]
	v_mfma_f32_32x32x16_f16 v[34:49], v[134:137], v[166:169], v[34:49]
	ds_read_b128 v[134:137], v236 offset:4480
	s_waitcnt lgkmcnt(3)
	v_mfma_f32_32x32x16_f16 v[98:113], v[138:141], v[162:165], v[98:113]
	v_mfma_f32_32x32x16_f16 v[18:33], v[138:141], v[166:169], v[18:33]
	ds_read_b128 v[138:141], v236 offset:8832
	s_waitcnt lgkmcnt(3)
	v_mfma_f32_32x32x16_f16 v[66:81], v[142:145], v[162:165], v[66:81]
	v_mfma_f32_32x32x16_f16 v[2:17], v[142:145], v[166:169], v[2:17]
	ds_read_b128 v[142:145], v236 offset:13184
	global_load_dwordx4 v[162:165], v239, s[56:57]
	global_load_dwordx4 v[166:169], v239, s[56:57] offset:512
	s_add_u32 s56, s56, 0x4000
	s_addc_u32 s57, s57, 0
	s_waitcnt vmcnt(20)
	s_waitcnt lgkmcnt(3)
	v_mfma_f32_32x32x16_f16 v[82:97], v[130:133], v[170:173], v[82:97]
	v_mfma_f32_32x32x16_f16 v[50:65], v[130:133], v[174:177], v[50:65]
	ds_read_b128 v[130:133], v236 offset:160
	s_waitcnt lgkmcnt(3)
	v_mfma_f32_32x32x16_f16 v[114:129], v[134:137], v[170:173], v[114:129]
	v_mfma_f32_32x32x16_f16 v[34:49], v[134:137], v[174:177], v[34:49]
	ds_read_b128 v[134:137], v236 offset:4512
	s_waitcnt lgkmcnt(3)
	v_mfma_f32_32x32x16_f16 v[98:113], v[138:141], v[170:173], v[98:113]
	v_mfma_f32_32x32x16_f16 v[18:33], v[138:141], v[174:177], v[18:33]
	ds_read_b128 v[138:141], v236 offset:8864
	s_waitcnt lgkmcnt(3)
	v_mfma_f32_32x32x16_f16 v[66:81], v[142:145], v[170:173], v[66:81]
	v_mfma_f32_32x32x16_f16 v[2:17], v[142:145], v[174:177], v[2:17]
	ds_read_b128 v[142:145], v236 offset:13216
	global_load_dwordx4 v[170:173], v239, s[56:57]
	global_load_dwordx4 v[174:177], v239, s[56:57] offset:512
	s_add_u32 s56, s56, 0x4000
	s_addc_u32 s57, s57, 0
	s_waitcnt vmcnt(12)
	s_waitcnt lgkmcnt(3)
	v_mfma_f32_32x32x16_f16 v[82:97], v[130:133], v[178:181], v[82:97]
	v_mfma_f32_32x32x16_f16 v[50:65], v[130:133], v[182:185], v[50:65]
	ds_read_b128 v[130:133], v236 offset:192
	s_waitcnt lgkmcnt(3)
	v_mfma_f32_32x32x16_f16 v[114:129], v[134:137], v[178:181], v[114:129]
	v_mfma_f32_32x32x16_f16 v[34:49], v[134:137], v[182:185], v[34:49]
	ds_read_b128 v[134:137], v236 offset:4544
	s_waitcnt lgkmcnt(3)
	v_mfma_f32_32x32x16_f16 v[98:113], v[138:141], v[178:181], v[98:113]
	v_mfma_f32_32x32x16_f16 v[18:33], v[138:141], v[182:185], v[18:33]
	ds_read_b128 v[138:141], v236 offset:8896
	s_waitcnt lgkmcnt(3)
	v_mfma_f32_32x32x16_f16 v[66:81], v[142:145], v[178:181], v[66:81]
	v_mfma_f32_32x32x16_f16 v[2:17], v[142:145], v[182:185], v[2:17]
	ds_read_b128 v[142:145], v236 offset:13248
	global_load_dwordx4 v[178:181], v239, s[56:57]
	global_load_dwordx4 v[182:185], v239, s[56:57] offset:512
	s_add_u32 s56, s56, 0x4000
	s_addc_u32 s57, s57, 0
	s_waitcnt vmcnt(23)
	v_cvt_pk_f16_f32 v204, v204, v205
	v_cvt_pk_f16_f32 v205, v206, v207
	ds_write_b64 v237, v[204:205] offset:34816
	s_waitcnt vmcnt(22)
	v_cvt_pk_f16_f32 v208, v208, v209
	v_cvt_pk_f16_f32 v209, v210, v211
	ds_write_b64 v237, v[208:209] offset:39168
	s_waitcnt vmcnt(21)
	v_cvt_pk_f16_f32 v212, v212, v213
	v_cvt_pk_f16_f32 v213, v214, v215
	ds_write_b64 v237, v[212:213] offset:43520
	s_waitcnt vmcnt(20)
	v_cvt_pk_f16_f32 v216, v216, v217
	v_cvt_pk_f16_f32 v217, v218, v219
	ds_write_b64 v237, v[216:217] offset:47872
	s_waitcnt vmcnt(19)
	v_cvt_pk_f16_f32 v220, v220, v221
	v_cvt_pk_f16_f32 v221, v222, v223
	ds_write_b64 v237, v[220:221] offset:52224
	s_waitcnt vmcnt(18)
	v_cvt_pk_f16_f32 v224, v224, v225
	v_cvt_pk_f16_f32 v225, v226, v227
	ds_write_b64 v237, v[224:225] offset:56576
	s_waitcnt vmcnt(17)
	v_cvt_pk_f16_f32 v228, v228, v229
	v_cvt_pk_f16_f32 v229, v230, v231
	ds_write_b64 v237, v[228:229] offset:60928
	s_waitcnt vmcnt(16)
	v_cvt_pk_f16_f32 v232, v232, v233
	v_cvt_pk_f16_f32 v233, v234, v235
	ds_write_b64 v237, v[232:233] offset:65280
	s_waitcnt vmcnt(12)
	s_waitcnt lgkmcnt(11)
	v_mfma_f32_32x32x16_f16 v[82:97], v[130:133], v[186:189], v[82:97]
	v_mfma_f32_32x32x16_f16 v[50:65], v[130:133], v[190:193], v[50:65]
	ds_read_b128 v[130:133], v236 offset:224
	s_waitcnt lgkmcnt(11)
	v_mfma_f32_32x32x16_f16 v[114:129], v[134:137], v[186:189], v[114:129]
	v_mfma_f32_32x32x16_f16 v[34:49], v[134:137], v[190:193], v[34:49]
	ds_read_b128 v[134:137], v236 offset:4576
	s_waitcnt lgkmcnt(11)
	v_mfma_f32_32x32x16_f16 v[98:113], v[138:141], v[186:189], v[98:113]
	v_mfma_f32_32x32x16_f16 v[18:33], v[138:141], v[190:193], v[18:33]
	ds_read_b128 v[138:141], v236 offset:8928
	s_waitcnt lgkmcnt(11)
	v_mfma_f32_32x32x16_f16 v[66:81], v[142:145], v[186:189], v[66:81]
	v_mfma_f32_32x32x16_f16 v[2:17], v[142:145], v[190:193], v[2:17]
	ds_read_b128 v[142:145], v236 offset:13280
	global_load_dwordx4 v[186:189], v239, s[56:57]
	global_load_dwordx4 v[190:193], v239, s[56:57] offset:512
	s_add_u32 s56, s56, 0x4000
	s_addc_u32 s57, s57, 0
	s_waitcnt vmcnt(12)
	s_waitcnt lgkmcnt(3)
	v_mfma_f32_32x32x16_f16 v[82:97], v[130:133], v[194:197], v[82:97]
	v_mfma_f32_32x32x16_f16 v[50:65], v[130:133], v[198:201], v[50:65]
	s_waitcnt lgkmcnt(2)
	v_mfma_f32_32x32x16_f16 v[114:129], v[134:137], v[194:197], v[114:129]
	v_mfma_f32_32x32x16_f16 v[34:49], v[134:137], v[198:201], v[34:49]
	s_waitcnt lgkmcnt(1)
	v_mfma_f32_32x32x16_f16 v[98:113], v[138:141], v[194:197], v[98:113]
	v_mfma_f32_32x32x16_f16 v[18:33], v[138:141], v[198:201], v[18:33]
	s_waitcnt lgkmcnt(0)
	v_mfma_f32_32x32x16_f16 v[66:81], v[142:145], v[194:197], v[66:81]
	v_mfma_f32_32x32x16_f16 v[2:17], v[142:145], v[198:201], v[2:17]
	global_load_dwordx4 v[194:197], v239, s[56:57]
	global_load_dwordx4 v[198:201], v239, s[56:57] offset:512
	s_add_u32 s56, s56, 0x4000
	s_addc_u32 s57, s57, 0
	s_waitcnt lgkmcnt(0)
	s_barrier
	ds_read_b128 v[130:133], v236 offset:34816
	ds_read_b128 v[134:137], v236 offset:39168
	ds_read_b128 v[138:141], v236 offset:43520
	ds_read_b128 v[142:145], v236 offset:47872
	s_waitcnt vmcnt(12)
	s_waitcnt lgkmcnt(3)
	v_mfma_f32_32x32x16_f16 v[82:97], v[130:133], v[146:149], v[82:97]
	v_mfma_f32_32x32x16_f16 v[50:65], v[130:133], v[150:153], v[50:65]
	ds_read_b128 v[130:133], v236 offset:34848
	s_waitcnt lgkmcnt(3)
	v_mfma_f32_32x32x16_f16 v[114:129], v[134:137], v[146:149], v[114:129]
	v_mfma_f32_32x32x16_f16 v[34:49], v[134:137], v[150:153], v[34:49]
	ds_read_b128 v[134:137], v236 offset:39200
	s_waitcnt lgkmcnt(3)
	v_mfma_f32_32x32x16_f16 v[98:113], v[138:141], v[146:149], v[98:113]
	v_mfma_f32_32x32x16_f16 v[18:33], v[138:141], v[150:153], v[18:33]
	ds_read_b128 v[138:141], v236 offset:43552
	s_waitcnt lgkmcnt(3)
	v_mfma_f32_32x32x16_f16 v[66:81], v[142:145], v[146:149], v[66:81]
	v_mfma_f32_32x32x16_f16 v[2:17], v[142:145], v[150:153], v[2:17]
	ds_read_b128 v[142:145], v236 offset:47904
	global_load_dwordx4 v[146:149], v239, s[56:57]
	global_load_dwordx4 v[150:153], v239, s[56:57] offset:512
	s_add_u32 s56, s56, 0x4000
	s_addc_u32 s57, s57, 0
	s_waitcnt vmcnt(12)
	s_waitcnt lgkmcnt(3)
	v_mfma_f32_32x32x16_f16 v[82:97], v[130:133], v[154:157], v[82:97]
	v_mfma_f32_32x32x16_f16 v[50:65], v[130:133], v[158:161], v[50:65]
	ds_read_b128 v[130:133], v236 offset:34880
	s_waitcnt lgkmcnt(3)
	v_mfma_f32_32x32x16_f16 v[114:129], v[134:137], v[154:157], v[114:129]
	v_mfma_f32_32x32x16_f16 v[34:49], v[134:137], v[158:161], v[34:49]
	ds_read_b128 v[134:137], v236 offset:39232
	s_waitcnt lgkmcnt(3)
	v_mfma_f32_32x32x16_f16 v[98:113], v[138:141], v[154:157], v[98:113]
	v_mfma_f32_32x32x16_f16 v[18:33], v[138:141], v[158:161], v[18:33]
	ds_read_b128 v[138:141], v236 offset:43584
	s_waitcnt lgkmcnt(3)
	v_mfma_f32_32x32x16_f16 v[66:81], v[142:145], v[154:157], v[66:81]
	v_mfma_f32_32x32x16_f16 v[2:17], v[142:145], v[158:161], v[2:17]
	ds_read_b128 v[142:145], v236 offset:47936
	s_waitcnt vmcnt(10)
	s_waitcnt lgkmcnt(3)
	v_mfma_f32_32x32x16_f16 v[82:97], v[130:133], v[162:165], v[82:97]
	v_mfma_f32_32x32x16_f16 v[50:65], v[130:133], v[166:169], v[50:65]
	ds_read_b128 v[130:133], v236 offset:34912
	s_waitcnt lgkmcnt(3)
	v_mfma_f32_32x32x16_f16 v[114:129], v[134:137], v[162:165], v[114:129]
	v_mfma_f32_32x32x16_f16 v[34:49], v[134:137], v[166:169], v[34:49]
	ds_read_b128 v[134:137], v236 offset:39264
	s_waitcnt lgkmcnt(3)
	v_mfma_f32_32x32x16_f16 v[98:113], v[138:141], v[162:165], v[98:113]
	v_mfma_f32_32x32x16_f16 v[18:33], v[138:141], v[166:169], v[18:33]
	ds_read_b128 v[138:141], v236 offset:43616
	s_waitcnt lgkmcnt(3)
	v_mfma_f32_32x32x16_f16 v[66:81], v[142:145], v[162:165], v[66:81]
	v_mfma_f32_32x32x16_f16 v[2:17], v[142:145], v[166:169], v[2:17]
	ds_read_b128 v[142:145], v236 offset:47968
	s_waitcnt vmcnt(8)
	s_waitcnt lgkmcnt(3)
	v_mfma_f32_32x32x16_f16 v[82:97], v[130:133], v[170:173], v[82:97]
	v_mfma_f32_32x32x16_f16 v[50:65], v[130:133], v[174:177], v[50:65]
	ds_read_b128 v[130:133], v236 offset:34944
	s_waitcnt lgkmcnt(3)
	v_mfma_f32_32x32x16_f16 v[114:129], v[134:137], v[170:173], v[114:129]
	v_mfma_f32_32x32x16_f16 v[34:49], v[134:137], v[174:177], v[34:49]
	ds_read_b128 v[134:137], v236 offset:39296
	s_waitcnt lgkmcnt(3)
	v_mfma_f32_32x32x16_f16 v[98:113], v[138:141], v[170:173], v[98:113]
	v_mfma_f32_32x32x16_f16 v[18:33], v[138:141], v[174:177], v[18:33]
	ds_read_b128 v[138:141], v236 offset:43648
	s_waitcnt lgkmcnt(3)
	v_mfma_f32_32x32x16_f16 v[66:81], v[142:145], v[170:173], v[66:81]
	v_mfma_f32_32x32x16_f16 v[2:17], v[142:145], v[174:177], v[2:17]
	ds_read_b128 v[142:145], v236 offset:48000
	s_waitcnt vmcnt(6)
	s_waitcnt lgkmcnt(3)
	v_mfma_f32_32x32x16_f16 v[82:97], v[130:133], v[178:181], v[82:97]
	v_mfma_f32_32x32x16_f16 v[50:65], v[130:133], v[182:185], v[50:65]
	ds_read_b128 v[130:133], v236 offset:34976
	s_waitcnt lgkmcnt(3)
	v_mfma_f32_32x32x16_f16 v[114:129], v[134:137], v[178:181], v[114:129]
	v_mfma_f32_32x32x16_f16 v[34:49], v[134:137], v[182:185], v[34:49]
	ds_read_b128 v[134:137], v236 offset:39328
	s_waitcnt lgkmcnt(3)
	v_mfma_f32_32x32x16_f16 v[98:113], v[138:141], v[178:181], v[98:113]
	v_mfma_f32_32x32x16_f16 v[18:33], v[138:141], v[182:185], v[18:33]
	ds_read_b128 v[138:141], v236 offset:43680
	s_waitcnt lgkmcnt(3)
	v_mfma_f32_32x32x16_f16 v[66:81], v[142:145], v[178:181], v[66:81]
	v_mfma_f32_32x32x16_f16 v[2:17], v[142:145], v[182:185], v[2:17]
	ds_read_b128 v[142:145], v236 offset:48032
	s_waitcnt vmcnt(4)
	s_waitcnt lgkmcnt(3)
	v_mfma_f32_32x32x16_f16 v[82:97], v[130:133], v[186:189], v[82:97]
	v_mfma_f32_32x32x16_f16 v[50:65], v[130:133], v[190:193], v[50:65]
	ds_read_b128 v[130:133], v236 offset:35008
	s_waitcnt lgkmcnt(3)
	v_mfma_f32_32x32x16_f16 v[114:129], v[134:137], v[186:189], v[114:129]
	v_mfma_f32_32x32x16_f16 v[34:49], v[134:137], v[190:193], v[34:49]
	ds_read_b128 v[134:137], v236 offset:39360
	s_waitcnt lgkmcnt(3)
	v_mfma_f32_32x32x16_f16 v[98:113], v[138:141], v[186:189], v[98:113]
	v_mfma_f32_32x32x16_f16 v[18:33], v[138:141], v[190:193], v[18:33]
	ds_read_b128 v[138:141], v236 offset:43712
	s_waitcnt lgkmcnt(3)
	v_mfma_f32_32x32x16_f16 v[66:81], v[142:145], v[186:189], v[66:81]
	v_mfma_f32_32x32x16_f16 v[2:17], v[142:145], v[190:193], v[2:17]
	ds_read_b128 v[142:145], v236 offset:48064
	s_waitcnt vmcnt(2)
	s_waitcnt lgkmcnt(3)
	v_mfma_f32_32x32x16_f16 v[82:97], v[130:133], v[194:197], v[82:97]
	v_mfma_f32_32x32x16_f16 v[50:65], v[130:133], v[198:201], v[50:65]
	ds_read_b128 v[130:133], v236 offset:35040
	s_waitcnt lgkmcnt(3)
	v_mfma_f32_32x32x16_f16 v[114:129], v[134:137], v[194:197], v[114:129]
	v_mfma_f32_32x32x16_f16 v[34:49], v[134:137], v[198:201], v[34:49]
	ds_read_b128 v[134:137], v236 offset:39392
	s_waitcnt lgkmcnt(3)
	v_mfma_f32_32x32x16_f16 v[98:113], v[138:141], v[194:197], v[98:113]
	v_mfma_f32_32x32x16_f16 v[18:33], v[138:141], v[198:201], v[18:33]
	ds_read_b128 v[138:141], v236 offset:43744
	s_waitcnt lgkmcnt(3)
	v_mfma_f32_32x32x16_f16 v[66:81], v[142:145], v[194:197], v[66:81]
	v_mfma_f32_32x32x16_f16 v[2:17], v[142:145], v[198:201], v[2:17]
	ds_read_b128 v[142:145], v236 offset:48096
	s_waitcnt vmcnt(0)
	s_waitcnt lgkmcnt(3)
	v_mfma_f32_32x32x16_f16 v[82:97], v[130:133], v[146:149], v[82:97]
	v_mfma_f32_32x32x16_f16 v[50:65], v[130:133], v[150:153], v[50:65]
	s_waitcnt lgkmcnt(2)
	v_mfma_f32_32x32x16_f16 v[114:129], v[134:137], v[146:149], v[114:129]
	v_mfma_f32_32x32x16_f16 v[34:49], v[134:137], v[150:153], v[34:49]
	s_waitcnt lgkmcnt(1)
	v_mfma_f32_32x32x16_f16 v[98:113], v[138:141], v[146:149], v[98:113]
	v_mfma_f32_32x32x16_f16 v[18:33], v[138:141], v[150:153], v[18:33]
	s_waitcnt lgkmcnt(0)
	v_mfma_f32_32x32x16_f16 v[66:81], v[142:145], v[146:149], v[66:81]
	v_mfma_f32_32x32x16_f16 v[2:17], v[142:145], v[150:153], v[2:17]
	s_waitcnt vmcnt(0) lgkmcnt(0)
	s_nop 15
	s_mov_b64 exec, -1
	v_bfe_u32 v202, v0, 5, 1
	s_lshl_b32 s34, s29, 9
	v_and_b32_e32 v203, 0x1c0, v0
	v_and_b32_e32 v204, 31, v0
	v_or3_b32 v0, s34, v203, v204
	v_lshlrev_b32_e32 v0, 2, v0
	s_waitcnt vmcnt(0) lgkmcnt(0)
	s_barrier
	v_mov_b32_e32 v131, v244
	v_mov_b32_e32 v1, v245
	s_mov_b32 s6, 0x3dcccccd
	s_mov_b32 s7, 0xbdcccccd
	v_mov_b32_e32 v132, 0
	v_mov_b32_e32 v133, 0
	v_mov_b32_e32 v134, 0
	v_mov_b32_e32 v135, 0
	v_fma_f32 v130, -v133, v131, v82
	v_fma_f32 v246, -v135, v1, v50
	v_fmac_f32_e32 v132, 0x3dcccccd, v130
	v_fmac_f32_e32 v134, 0x3dcccccd, v246
	v_fmac_f32_e32 v133, 0x3dcccccd, v132
	v_fmac_f32_e32 v135, 0x3dcccccd, v134
	v_fma_f32 v130, -v133, v131, v83
	v_fma_f32 v246, -v135, v1, v51
	v_fmac_f32_e32 v132, 0x3dcccccd, v130
	v_fmac_f32_e32 v134, 0x3dcccccd, v246
	v_fmac_f32_e32 v133, 0x3dcccccd, v132
	v_fmac_f32_e32 v135, 0x3dcccccd, v134
	v_fma_f32 v130, -v133, v131, v84
	v_fma_f32 v246, -v135, v1, v52
	v_fmac_f32_e32 v132, 0x3dcccccd, v130
	v_fmac_f32_e32 v134, 0x3dcccccd, v246
	v_fmac_f32_e32 v133, 0x3dcccccd, v132
	v_fmac_f32_e32 v135, 0x3dcccccd, v134
	v_fma_f32 v130, -v133, v131, v85
	v_fma_f32 v246, -v135, v1, v53
	v_fmac_f32_e32 v132, 0x3dcccccd, v130
	v_fmac_f32_e32 v134, 0x3dcccccd, v246
	v_fmac_f32_e32 v133, 0x3dcccccd, v132
	v_fmac_f32_e32 v135, 0x3dcccccd, v134
	v_fma_f32 v130, -v133, v131, v86
	v_fma_f32 v246, -v135, v1, v54
	v_fmac_f32_e32 v132, 0x3dcccccd, v130
	v_fmac_f32_e32 v134, 0x3dcccccd, v246
	v_fmac_f32_e32 v133, 0x3dcccccd, v132
	v_fmac_f32_e32 v135, 0x3dcccccd, v134
	v_fma_f32 v130, -v133, v131, v87
	v_fma_f32 v246, -v135, v1, v55
	v_fmac_f32_e32 v132, 0x3dcccccd, v130
	v_fmac_f32_e32 v134, 0x3dcccccd, v246
	v_fmac_f32_e32 v133, 0x3dcccccd, v132
	v_fmac_f32_e32 v135, 0x3dcccccd, v134
	v_fma_f32 v130, -v133, v131, v88
	v_fma_f32 v246, -v135, v1, v56
	v_fmac_f32_e32 v132, 0x3dcccccd, v130
	v_fmac_f32_e32 v134, 0x3dcccccd, v246
	v_fmac_f32_e32 v133, 0x3dcccccd, v132
	v_fmac_f32_e32 v135, 0x3dcccccd, v134
	v_fma_f32 v130, -v133, v131, v89
	v_fma_f32 v246, -v135, v1, v57
	v_fmac_f32_e32 v132, 0x3dcccccd, v130
	v_fmac_f32_e32 v134, 0x3dcccccd, v246
	v_fmac_f32_e32 v133, 0x3dcccccd, v132
	v_fmac_f32_e32 v135, 0x3dcccccd, v134
	v_fma_f32 v130, -v133, v131, v90
	v_fma_f32 v246, -v135, v1, v58
	v_fmac_f32_e32 v132, 0x3dcccccd, v130
	v_fmac_f32_e32 v134, 0x3dcccccd, v246
	v_fmac_f32_e32 v133, 0x3dcccccd, v132
	v_fmac_f32_e32 v135, 0x3dcccccd, v134
	v_fma_f32 v130, -v133, v131, v91
	v_fma_f32 v246, -v135, v1, v59
	v_fmac_f32_e32 v132, 0x3dcccccd, v130
	v_fmac_f32_e32 v134, 0x3dcccccd, v246
	v_fmac_f32_e32 v133, 0x3dcccccd, v132
	v_fmac_f32_e32 v135, 0x3dcccccd, v134
	v_fma_f32 v130, -v133, v131, v92
	v_fma_f32 v246, -v135, v1, v60
	v_fmac_f32_e32 v132, 0x3dcccccd, v130
	v_fmac_f32_e32 v134, 0x3dcccccd, v246
	v_fmac_f32_e32 v133, 0x3dcccccd, v132
	v_fmac_f32_e32 v135, 0x3dcccccd, v134
	v_fma_f32 v130, -v133, v131, v93
	v_fma_f32 v246, -v135, v1, v61
	v_fmac_f32_e32 v132, 0x3dcccccd, v130
	v_fmac_f32_e32 v134, 0x3dcccccd, v246
	v_fmac_f32_e32 v133, 0x3dcccccd, v132
	v_fmac_f32_e32 v135, 0x3dcccccd, v134
	v_fma_f32 v130, -v133, v131, v94
	v_fma_f32 v246, -v135, v1, v62
	v_fmac_f32_e32 v132, 0x3dcccccd, v130
	v_fmac_f32_e32 v134, 0x3dcccccd, v246
	v_fmac_f32_e32 v133, 0x3dcccccd, v132
	v_fmac_f32_e32 v135, 0x3dcccccd, v134
	v_fma_f32 v130, -v133, v131, v95
	v_fma_f32 v246, -v135, v1, v63
	v_fmac_f32_e32 v132, 0x3dcccccd, v130
	v_fmac_f32_e32 v134, 0x3dcccccd, v246
	v_fmac_f32_e32 v133, 0x3dcccccd, v132
	v_fmac_f32_e32 v135, 0x3dcccccd, v134
	v_fma_f32 v130, -v133, v131, v96
	v_fma_f32 v246, -v135, v1, v64
	v_fmac_f32_e32 v132, 0x3dcccccd, v130
	v_fmac_f32_e32 v134, 0x3dcccccd, v246
	v_fmac_f32_e32 v133, 0x3dcccccd, v132
	v_fmac_f32_e32 v135, 0x3dcccccd, v134
	v_fma_f32 v130, -v133, v131, v97
	v_fma_f32 v246, -v135, v1, v65
	v_fmac_f32_e32 v132, 0x3dcccccd, v130
	v_fmac_f32_e32 v134, 0x3dcccccd, v246
	v_fmac_f32_e32 v133, 0x3dcccccd, v132
	v_fmac_f32_e32 v135, 0x3dcccccd, v134
	v_fma_f32 v130, -v133, v131, v114
	v_fma_f32 v246, -v135, v1, v34
	v_fmac_f32_e32 v132, 0x3dcccccd, v130
	v_fmac_f32_e32 v134, 0x3dcccccd, v246
	v_fmac_f32_e32 v133, 0x3dcccccd, v132
	v_fmac_f32_e32 v135, 0x3dcccccd, v134
	v_fma_f32 v130, -v133, v131, v115
	v_fma_f32 v246, -v135, v1, v35
	v_fmac_f32_e32 v132, 0x3dcccccd, v130
	v_fmac_f32_e32 v134, 0x3dcccccd, v246
	v_fmac_f32_e32 v133, 0x3dcccccd, v132
	v_fmac_f32_e32 v135, 0x3dcccccd, v134
	v_fma_f32 v130, -v133, v131, v116
	v_fma_f32 v246, -v135, v1, v36
	v_fmac_f32_e32 v132, 0x3dcccccd, v130
	v_fmac_f32_e32 v134, 0x3dcccccd, v246
	v_fmac_f32_e32 v133, 0x3dcccccd, v132
	v_fmac_f32_e32 v135, 0x3dcccccd, v134
	v_fma_f32 v130, -v133, v131, v117
	v_fma_f32 v246, -v135, v1, v37
	v_fmac_f32_e32 v132, 0x3dcccccd, v130
	v_fmac_f32_e32 v134, 0x3dcccccd, v246
	v_fmac_f32_e32 v133, 0x3dcccccd, v132
	v_fmac_f32_e32 v135, 0x3dcccccd, v134
	v_fma_f32 v130, -v133, v131, v118
	v_fma_f32 v246, -v135, v1, v38
	v_fmac_f32_e32 v132, 0x3dcccccd, v130
	v_fmac_f32_e32 v134, 0x3dcccccd, v246
	v_fmac_f32_e32 v133, 0x3dcccccd, v132
	v_fmac_f32_e32 v135, 0x3dcccccd, v134
	v_fma_f32 v130, -v133, v131, v119
	v_fma_f32 v246, -v135, v1, v39
	v_fmac_f32_e32 v132, 0x3dcccccd, v130
	v_fmac_f32_e32 v134, 0x3dcccccd, v246
	v_fmac_f32_e32 v133, 0x3dcccccd, v132
	v_fmac_f32_e32 v135, 0x3dcccccd, v134
	v_fma_f32 v130, -v133, v131, v120
	v_fma_f32 v246, -v135, v1, v40
	v_fmac_f32_e32 v132, 0x3dcccccd, v130
	v_fmac_f32_e32 v134, 0x3dcccccd, v246
	v_fmac_f32_e32 v133, 0x3dcccccd, v132
	v_fmac_f32_e32 v135, 0x3dcccccd, v134
	v_fma_f32 v130, -v133, v131, v121
	v_fma_f32 v246, -v135, v1, v41
	v_fmac_f32_e32 v132, 0x3dcccccd, v130
	v_fmac_f32_e32 v134, 0x3dcccccd, v246
	v_fmac_f32_e32 v133, 0x3dcccccd, v132
	v_fmac_f32_e32 v135, 0x3dcccccd, v134
	v_fma_f32 v130, -v133, v131, v122
	v_fma_f32 v246, -v135, v1, v42
	v_fmac_f32_e32 v132, 0x3dcccccd, v130
	v_fmac_f32_e32 v134, 0x3dcccccd, v246
	v_fmac_f32_e32 v133, 0x3dcccccd, v132
	v_fmac_f32_e32 v135, 0x3dcccccd, v134
	v_fma_f32 v130, -v133, v131, v123
	v_fma_f32 v246, -v135, v1, v43
	v_fmac_f32_e32 v132, 0x3dcccccd, v130
	v_fmac_f32_e32 v134, 0x3dcccccd, v246
	v_fmac_f32_e32 v133, 0x3dcccccd, v132
	v_fmac_f32_e32 v135, 0x3dcccccd, v134
	v_fma_f32 v130, -v133, v131, v124
	v_fma_f32 v246, -v135, v1, v44
	v_fmac_f32_e32 v132, 0x3dcccccd, v130
	v_fmac_f32_e32 v134, 0x3dcccccd, v246
	v_fmac_f32_e32 v133, 0x3dcccccd, v132
	v_fmac_f32_e32 v135, 0x3dcccccd, v134
	v_fma_f32 v130, -v133, v131, v125
	v_fma_f32 v246, -v135, v1, v45
	v_fmac_f32_e32 v132, 0x3dcccccd, v130
	v_fmac_f32_e32 v134, 0x3dcccccd, v246
	v_fmac_f32_e32 v133, 0x3dcccccd, v132
	v_fmac_f32_e32 v135, 0x3dcccccd, v134
	v_fma_f32 v130, -v133, v131, v126
	v_fma_f32 v246, -v135, v1, v46
	v_fmac_f32_e32 v132, 0x3dcccccd, v130
	v_fmac_f32_e32 v134, 0x3dcccccd, v246
	v_fmac_f32_e32 v133, 0x3dcccccd, v132
	v_fmac_f32_e32 v135, 0x3dcccccd, v134
	v_fma_f32 v130, -v133, v131, v127
	v_fma_f32 v246, -v135, v1, v47
	v_fmac_f32_e32 v132, 0x3dcccccd, v130
	v_fmac_f32_e32 v134, 0x3dcccccd, v246
	v_fmac_f32_e32 v133, 0x3dcccccd, v132
	v_fmac_f32_e32 v135, 0x3dcccccd, v134
	v_fma_f32 v130, -v133, v131, v128
	v_fma_f32 v246, -v135, v1, v48
	v_fmac_f32_e32 v132, 0x3dcccccd, v130
	v_fmac_f32_e32 v134, 0x3dcccccd, v246
	v_fmac_f32_e32 v133, 0x3dcccccd, v132
	v_fmac_f32_e32 v135, 0x3dcccccd, v134
	v_fma_f32 v130, -v133, v131, v129
	v_fma_f32 v246, -v135, v1, v49
	v_fmac_f32_e32 v132, 0x3dcccccd, v130
	v_fmac_f32_e32 v134, 0x3dcccccd, v246
	v_fmac_f32_e32 v133, 0x3dcccccd, v132
	v_fmac_f32_e32 v135, 0x3dcccccd, v134
	v_fma_f32 v130, -v133, v131, v98
	v_fma_f32 v246, -v135, v1, v18
	v_fmac_f32_e32 v132, 0x3dcccccd, v130
	v_fmac_f32_e32 v134, 0x3dcccccd, v246
	v_fmac_f32_e32 v133, 0x3dcccccd, v132
	v_fmac_f32_e32 v135, 0x3dcccccd, v134
	v_fma_f32 v130, -v133, v131, v99
	v_fma_f32 v246, -v135, v1, v19
	v_fmac_f32_e32 v132, 0x3dcccccd, v130
	v_fmac_f32_e32 v134, 0x3dcccccd, v246
	v_fmac_f32_e32 v133, 0x3dcccccd, v132
	v_fmac_f32_e32 v135, 0x3dcccccd, v134
	v_fma_f32 v130, -v133, v131, v100
	v_fma_f32 v246, -v135, v1, v20
	v_fmac_f32_e32 v132, 0x3dcccccd, v130
	v_fmac_f32_e32 v134, 0x3dcccccd, v246
	v_fmac_f32_e32 v133, 0x3dcccccd, v132
	v_fmac_f32_e32 v135, 0x3dcccccd, v134
	v_fma_f32 v130, -v133, v131, v101
	v_fma_f32 v246, -v135, v1, v21
	v_fmac_f32_e32 v132, 0x3dcccccd, v130
	v_fmac_f32_e32 v134, 0x3dcccccd, v246
	v_fmac_f32_e32 v133, 0x3dcccccd, v132
	v_fmac_f32_e32 v135, 0x3dcccccd, v134
	v_fma_f32 v130, -v133, v131, v102
	v_fma_f32 v246, -v135, v1, v22
	v_fmac_f32_e32 v132, 0x3dcccccd, v130
	v_fmac_f32_e32 v134, 0x3dcccccd, v246
	v_fmac_f32_e32 v133, 0x3dcccccd, v132
	v_fmac_f32_e32 v135, 0x3dcccccd, v134
	v_fma_f32 v130, -v133, v131, v103
	v_fma_f32 v246, -v135, v1, v23
	v_fmac_f32_e32 v132, 0x3dcccccd, v130
	v_fmac_f32_e32 v134, 0x3dcccccd, v246
	v_fmac_f32_e32 v133, 0x3dcccccd, v132
	v_fmac_f32_e32 v135, 0x3dcccccd, v134
	v_fma_f32 v130, -v133, v131, v104
	v_fma_f32 v246, -v135, v1, v24
	v_fmac_f32_e32 v132, 0x3dcccccd, v130
	v_fmac_f32_e32 v134, 0x3dcccccd, v246
	v_fmac_f32_e32 v133, 0x3dcccccd, v132
	v_fmac_f32_e32 v135, 0x3dcccccd, v134
	v_fma_f32 v130, -v133, v131, v105
	v_fma_f32 v246, -v135, v1, v25
	v_fmac_f32_e32 v132, 0x3dcccccd, v130
	v_fmac_f32_e32 v134, 0x3dcccccd, v246
	v_fmac_f32_e32 v133, 0x3dcccccd, v132
	v_fmac_f32_e32 v135, 0x3dcccccd, v134
	v_fma_f32 v130, -v133, v131, v106
	v_fma_f32 v246, -v135, v1, v26
	v_fmac_f32_e32 v132, 0x3dcccccd, v130
	v_fmac_f32_e32 v134, 0x3dcccccd, v246
	v_fmac_f32_e32 v133, 0x3dcccccd, v132
	v_fmac_f32_e32 v135, 0x3dcccccd, v134
	v_fma_f32 v130, -v133, v131, v107
	v_fma_f32 v246, -v135, v1, v27
	v_fmac_f32_e32 v132, 0x3dcccccd, v130
	v_fmac_f32_e32 v134, 0x3dcccccd, v246
	v_fmac_f32_e32 v133, 0x3dcccccd, v132
	v_fmac_f32_e32 v135, 0x3dcccccd, v134
	v_fma_f32 v130, -v133, v131, v108
	v_fma_f32 v246, -v135, v1, v28
	v_fmac_f32_e32 v132, 0x3dcccccd, v130
	v_fmac_f32_e32 v134, 0x3dcccccd, v246
	v_fmac_f32_e32 v133, 0x3dcccccd, v132
	v_fmac_f32_e32 v135, 0x3dcccccd, v134
	v_fma_f32 v130, -v133, v131, v109
	v_fma_f32 v246, -v135, v1, v29
	v_fmac_f32_e32 v132, 0x3dcccccd, v130
	v_fmac_f32_e32 v134, 0x3dcccccd, v246
	v_fmac_f32_e32 v133, 0x3dcccccd, v132
	v_fmac_f32_e32 v135, 0x3dcccccd, v134
	v_fma_f32 v130, -v133, v131, v110
	v_fma_f32 v246, -v135, v1, v30
	v_fmac_f32_e32 v132, 0x3dcccccd, v130
	v_fmac_f32_e32 v134, 0x3dcccccd, v246
	v_fmac_f32_e32 v133, 0x3dcccccd, v132
	v_fmac_f32_e32 v135, 0x3dcccccd, v134
	v_fma_f32 v130, -v133, v131, v111
	v_fma_f32 v246, -v135, v1, v31
	v_fmac_f32_e32 v132, 0x3dcccccd, v130
	v_fmac_f32_e32 v134, 0x3dcccccd, v246
	v_fmac_f32_e32 v133, 0x3dcccccd, v132
	v_fmac_f32_e32 v135, 0x3dcccccd, v134
	v_fma_f32 v130, -v133, v131, v112
	v_fma_f32 v246, -v135, v1, v32
	v_fmac_f32_e32 v132, 0x3dcccccd, v130
	v_fmac_f32_e32 v134, 0x3dcccccd, v246
	v_fmac_f32_e32 v133, 0x3dcccccd, v132
	v_fmac_f32_e32 v135, 0x3dcccccd, v134
	v_fma_f32 v130, -v133, v131, v113
	v_fma_f32 v246, -v135, v1, v33
	v_fmac_f32_e32 v132, 0x3dcccccd, v130
	v_fmac_f32_e32 v134, 0x3dcccccd, v246
	v_fmac_f32_e32 v133, 0x3dcccccd, v132
	v_fmac_f32_e32 v135, 0x3dcccccd, v134
	v_fma_f32 v130, -v133, v131, v66
	v_fma_f32 v246, -v135, v1, v2
	v_fmac_f32_e32 v132, 0x3dcccccd, v130
	v_fmac_f32_e32 v134, 0x3dcccccd, v246
	v_fmac_f32_e32 v133, 0x3dcccccd, v132
	v_fmac_f32_e32 v135, 0x3dcccccd, v134
	v_fma_f32 v130, -v133, v131, v67
	v_fma_f32 v246, -v135, v1, v3
	v_fmac_f32_e32 v132, 0x3dcccccd, v130
	v_fmac_f32_e32 v134, 0x3dcccccd, v246
	v_fmac_f32_e32 v133, 0x3dcccccd, v132
	v_fmac_f32_e32 v135, 0x3dcccccd, v134
	v_fma_f32 v130, -v133, v131, v68
	v_fma_f32 v246, -v135, v1, v4
	v_fmac_f32_e32 v132, 0x3dcccccd, v130
	v_fmac_f32_e32 v134, 0x3dcccccd, v246
	v_fmac_f32_e32 v133, 0x3dcccccd, v132
	v_fmac_f32_e32 v135, 0x3dcccccd, v134
	v_fma_f32 v130, -v133, v131, v69
	v_fma_f32 v246, -v135, v1, v5
	v_fmac_f32_e32 v132, 0x3dcccccd, v130
	v_fmac_f32_e32 v134, 0x3dcccccd, v246
	v_fmac_f32_e32 v133, 0x3dcccccd, v132
	v_fmac_f32_e32 v135, 0x3dcccccd, v134
	v_fma_f32 v130, -v133, v131, v70
	v_fma_f32 v246, -v135, v1, v6
	v_fmac_f32_e32 v132, 0x3dcccccd, v130
	v_fmac_f32_e32 v134, 0x3dcccccd, v246
	v_fmac_f32_e32 v133, 0x3dcccccd, v132
	v_fmac_f32_e32 v135, 0x3dcccccd, v134
	v_fma_f32 v130, -v133, v131, v71
	v_fma_f32 v246, -v135, v1, v7
	v_fmac_f32_e32 v132, 0x3dcccccd, v130
	v_fmac_f32_e32 v134, 0x3dcccccd, v246
	v_fmac_f32_e32 v133, 0x3dcccccd, v132
	v_fmac_f32_e32 v135, 0x3dcccccd, v134
	v_fma_f32 v130, -v133, v131, v72
	v_fma_f32 v246, -v135, v1, v8
	v_fmac_f32_e32 v132, 0x3dcccccd, v130
	v_fmac_f32_e32 v134, 0x3dcccccd, v246
	v_fmac_f32_e32 v133, 0x3dcccccd, v132
	v_fmac_f32_e32 v135, 0x3dcccccd, v134
	v_fma_f32 v130, -v133, v131, v73
	v_fma_f32 v246, -v135, v1, v9
	v_fmac_f32_e32 v132, 0x3dcccccd, v130
	v_fmac_f32_e32 v134, 0x3dcccccd, v246
	v_fmac_f32_e32 v133, 0x3dcccccd, v132
	v_fmac_f32_e32 v135, 0x3dcccccd, v134
	v_fma_f32 v130, -v133, v131, v74
	v_fma_f32 v246, -v135, v1, v10
	v_fmac_f32_e32 v132, 0x3dcccccd, v130
	v_fmac_f32_e32 v134, 0x3dcccccd, v246
	v_fmac_f32_e32 v133, 0x3dcccccd, v132
	v_fmac_f32_e32 v135, 0x3dcccccd, v134
	v_fma_f32 v130, -v133, v131, v75
	v_fma_f32 v246, -v135, v1, v11
	v_fmac_f32_e32 v132, 0x3dcccccd, v130
	v_fmac_f32_e32 v134, 0x3dcccccd, v246
	v_fmac_f32_e32 v133, 0x3dcccccd, v132
	v_fmac_f32_e32 v135, 0x3dcccccd, v134
	v_fma_f32 v130, -v133, v131, v76
	v_fma_f32 v246, -v135, v1, v12
	v_fmac_f32_e32 v132, 0x3dcccccd, v130
	v_fmac_f32_e32 v134, 0x3dcccccd, v246
	v_fmac_f32_e32 v133, 0x3dcccccd, v132
	v_fmac_f32_e32 v135, 0x3dcccccd, v134
	v_fma_f32 v130, -v133, v131, v77
	v_fma_f32 v246, -v135, v1, v13
	v_fmac_f32_e32 v132, 0x3dcccccd, v130
	v_fmac_f32_e32 v134, 0x3dcccccd, v246
	v_fmac_f32_e32 v133, 0x3dcccccd, v132
	v_fmac_f32_e32 v135, 0x3dcccccd, v134
	v_fma_f32 v130, -v133, v131, v78
	v_fma_f32 v246, -v135, v1, v14
	v_fmac_f32_e32 v132, 0x3dcccccd, v130
	v_fmac_f32_e32 v134, 0x3dcccccd, v246
	v_fmac_f32_e32 v133, 0x3dcccccd, v132
	v_fmac_f32_e32 v135, 0x3dcccccd, v134
	v_fma_f32 v130, -v133, v131, v79
	v_fma_f32 v246, -v135, v1, v15
	v_fmac_f32_e32 v132, 0x3dcccccd, v130
	v_fmac_f32_e32 v134, 0x3dcccccd, v246
	v_fmac_f32_e32 v133, 0x3dcccccd, v132
	v_fmac_f32_e32 v135, 0x3dcccccd, v134
	v_fma_f32 v130, -v133, v131, v80
	v_fma_f32 v246, -v135, v1, v16
	v_fmac_f32_e32 v132, 0x3dcccccd, v130
	v_fmac_f32_e32 v134, 0x3dcccccd, v246
	v_fmac_f32_e32 v133, 0x3dcccccd, v132
	v_fmac_f32_e32 v135, 0x3dcccccd, v134
	v_fma_f32 v130, -v133, v131, v81
	v_fma_f32 v246, -v135, v1, v17
	v_fmac_f32_e32 v132, 0x3dcccccd, v130
	v_fmac_f32_e32 v134, 0x3dcccccd, v246
	v_fmac_f32_e32 v133, 0x3dcccccd, v132
	v_fmac_f32_e32 v135, 0x3dcccccd, v134
	v_lshlrev_b32_e32 v142, 3, v203
	v_lshlrev_b32_e32 v140, 3, v204
	v_add3_u32 v150, 0, v142, v140
	s_mov_b32 s10, 0xbc23d70b
	v_lshl_add_u32 v0, v202, 12, v150
	v_fma_f32 v130, v131, s10, 1.0
	ds_write2_b64 v0, v[132:133], v[134:135] offset1:32
	v_pk_mul_f32 v[132:133], v[130:131], s[6:7]
	s_lshl_b64 s[2:3], s[2:3], 13
	v_mov_b32_e32 v132, v130
	v_pk_mul_f32 v[136:137], v[132:133], s[6:7] op_sel_hi:[1,0]
	v_pk_mul_f32 v[138:139], v[130:131], v[132:133] op_sel_hi:[0,1]
	v_add_f32_e32 v0, 1.0, v137
	v_mov_b32_e32 v136, v137
	v_mov_b32_e32 v137, v133
	v_pk_fma_f32 v[144:145], v[130:131], v[132:133], v[136:137] op_sel_hi:[0,1,1]
	v_mov_b32_e32 v136, 0x3dcccccd
	v_mov_b32_e32 v137, v139
	v_pk_fma_f32 v[146:147], v[130:131], s[6:7], v[136:137]
	v_mov_b32_e32 v137, v138
	v_pk_fma_f32 v[132:133], v[132:133], s[6:7], v[136:137] op_sel_hi:[1,0,1]
	v_mov_b32_e32 v152, v144
	v_pk_mul_f32 v[132:133], v[144:145], v[132:133]
	v_mov_b32_e32 v145, v147
	v_mov_b32_e32 v153, v146
	v_mov_b32_e32 v138, v147
	v_mov_b32_e32 v139, v0
	v_mov_b32_e32 v148, v146
	v_mov_b32_e32 v149, v0
	v_pk_mul_f32 v[144:145], v[144:145], v[152:153]
	v_pk_fma_f32 v[132:133], v[0:1], v[146:147], v[132:133] op_sel_hi:[0,1,1]
	v_pk_fma_f32 v[138:139], v[138:139], v[148:149], v[144:145]
	s_add_u32 s8, s4, s2
	v_pk_mul_f32 v[144:145], v[132:133], v[138:139] op_sel_hi:[1,0]
	s_waitcnt lgkmcnt(0)
	v_pk_fma_f32 v[144:145], v[138:139], v[132:133], v[144:145] op_sel:[1,0,0]
	v_pk_mul_f32 v[132:133], v[132:133], v[132:133] op_sel:[1,0] op_sel_hi:[1,0]
	s_barrier
	v_pk_fma_f32 v[132:133], v[138:139], v[138:139], v[132:133]
	s_nop 0
	v_pk_mul_f32 v[138:139], v[144:145], v[132:133] op_sel_hi:[1,0]
	s_addc_u32 s3, s5, s3
	v_pk_fma_f32 v[138:139], v[132:133], v[144:145], v[138:139] op_sel:[1,0,0]
	v_pk_mul_f32 v[144:145], v[144:145], v[144:145] op_sel:[1,0] op_sel_hi:[1,0]
	s_lshl_b32 s2, s34, 3
	v_pk_fma_f32 v[132:133], v[132:133], v[132:133], v[144:145]
	ds_read_b64 v[148:149], v150
	v_pk_mul_f32 v[144:145], v[138:139], v[132:133] op_sel_hi:[1,0]
	s_add_u32 s8, s8, s2
	v_pk_fma_f32 v[144:145], v[132:133], v[138:139], v[144:145] op_sel:[1,0,0]
	v_pk_mul_f32 v[138:139], v[138:139], v[138:139] op_sel:[1,0] op_sel_hi:[1,0]
	v_mov_b32_e32 v143, 0
	v_pk_fma_f32 v[132:133], v[132:133], v[132:133], v[138:139]
	s_addc_u32 s9, s3, 0
	v_pk_mul_f32 v[138:139], v[132:133], v[132:133]
	v_pk_mul_f32 v[146:147], v[144:145], v[132:133] op_sel_hi:[1,0]
	v_mov_b32_e32 v141, v143
	v_pk_fma_f32 v[132:133], v[132:133], v[144:145], v[146:147] op_sel:[1,0,0]
	v_pk_fma_f32 v[146:147], v[144:145], v[144:145], v[138:139] op_sel:[1,0,0] op_sel_hi:[1,0,1]
	v_lshl_add_u64 v[138:139], s[8:9], 0, v[142:143]
	v_mov_b32_e32 v135, 1.0
	v_cmp_eq_u32_e64 s[0:1], 0, v202
	v_cmp_ne_u32_e32 vcc, 0, v202
	v_lshl_add_u64 v[144:145], v[138:139], 0, v[140:141]
	s_and_saveexec_b64 s[8:9], vcc
	s_cbranch_execz .LBB1_18
	ds_read_b64 v[138:139], v150 offset:4096
	v_mov_b32_e32 v152, v147
	v_mov_b32_e32 v153, v133
	s_waitcnt lgkmcnt(1)
	v_pk_mul_f32 v[152:153], v[148:149], v[152:153]
	s_nop 0
	v_add_f32_e32 v0, v152, v153
	v_mov_b32_e32 v152, v132
	v_mov_b32_e32 v153, v146
	v_pk_mul_f32 v[152:153], v[148:149], v[152:153]
	s_waitcnt lgkmcnt(0)
	v_add_f32_e32 v0, v138, v0
	v_add_f32_e32 v130, v152, v153
	v_add_f32_e32 v130, v139, v130
	v_or_b32_e32 v139, 1, v130
	v_or_b32_e32 v138, 1, v0
	global_store_dwordx2 v[144:145], v[138:139], off sc1

.LBB1_20:
	s_andn2_saveexec_b64 s[6:7], s[6:7]
	s_or_b64 exec, exec, s[6:7]
	v_lshlrev_b32_e32 v0, 4, v202
	v_or_b32_e32 v130, s28, v0
	v_lshlrev_b32_e32 v144, 13, v130
	v_or_b32_e32 v130, 1, v0
	v_cmp_gt_i32_e64 s[12:13], s33, v130
	v_or_b32_e32 v130, 2, v0
	v_mov_b32_e32 v145, 0
	v_cmp_gt_i32_e64 s[10:11], s33, v130
	v_or_b32_e32 v130, 3, v0
	s_mov_b32 s3, 0
	v_lshl_add_u64 v[150:151], s[4:5], 0, v[144:145]
	v_cmp_gt_i32_e64 s[8:9], s33, v130
	v_or_b32_e32 v130, 4, v0
	v_lshl_add_u64 v[150:151], v[150:151], 0, s[2:3]
	v_mov_b32_e32 v143, v145
	v_cmp_gt_i32_e64 s[6:7], s33, v130
	v_or_b32_e32 v130, 5, v0
	v_lshl_add_u64 v[142:143], v[150:151], 0, v[142:143]
	v_mov_b32_e32 v141, v145
	v_cmp_gt_i32_e64 s[4:5], s33, v130
	v_or_b32_e32 v130, 6, v0
	v_lshl_add_u64 v[158:159], v[142:143], 0, v[140:141]
	s_mov_b64 s[22:23], 0x2000
	s_mov_b32 s24, 1
	v_cmp_gt_i32_e64 s[2:3], s33, v130
	v_or_b32_e32 v130, 7, v0
	v_lshl_add_u64 v[140:141], v[158:159], 0, s[22:23]
	v_cmp_gt_i32_e64 s[14:15], s33, v0
	v_cmp_gt_i32_e32 vcc, s33, v130
	s_mov_b32 s35, 0x400000
	s_mov_b64 s[26:27], 0
	s_mov_b32 s25, s24
	s_sleep 30
	s_branch .LBB1_22

.LBB1_22:
	v_mov_b64_e32 v[142:143], v[140:141]
	global_load_dwordx2 v[184:185], v[158:159], off sc1
	global_load_dwordx2 v[156:157], v[158:159], off offset:256 sc1
	flat_load_dwordx2 v[182:183], v[142:143] sc1
	flat_load_dwordx2 v[186:187], v[142:143] offset:256 sc1
	v_lshl_add_u64 v[142:143], v[142:143], 0, s[22:23]
	flat_load_dwordx2 v[180:181], v[142:143] sc1
	flat_load_dwordx2 v[176:177], v[142:143] offset:256 sc1
	v_lshl_add_u64 v[142:143], v[142:143], 0, s[22:23]
	flat_load_dwordx2 v[178:179], v[142:143] sc1
	flat_load_dwordx2 v[174:175], v[142:143] offset:256 sc1
	v_lshl_add_u64 v[142:143], v[142:143], 0, s[22:23]
	flat_load_dwordx2 v[166:167], v[142:143] sc1
	flat_load_dwordx2 v[172:173], v[142:143] offset:256 sc1
	v_lshl_add_u64 v[142:143], v[142:143], 0, s[22:23]
	flat_load_dwordx2 v[164:165], v[142:143] sc1
	flat_load_dwordx2 v[170:171], v[142:143] offset:256 sc1
	v_lshl_add_u64 v[142:143], v[142:143], 0, s[22:23]
	flat_load_dwordx2 v[162:163], v[142:143] sc1
	flat_load_dwordx2 v[168:169], v[142:143] offset:256 sc1
	v_lshl_add_u64 v[142:143], v[142:143], 0, s[22:23]
	flat_load_dwordx2 v[160:161], v[142:143] sc1
	flat_load_dwordx2 v[144:145], v[142:143] offset:256 sc1
	v_lshl_add_u64 v[142:143], v[142:143], 0, s[22:23]
	s_or_b64 s[28:29], s[28:29], exec
	s_waitcnt vmcnt(0)
	v_and_b32_e32 v130, v157, v185
	v_and_b32_e32 v142, v156, v184
	s_waitcnt lgkmcnt(0)
	v_and_b32_e32 v143, v187, v183
	v_and_b32_e32 v150, v186, v182
	v_cndmask_b32_e64 v130, -1, v130, s[14:15]
	v_cndmask_b32_e64 v142, -1, v142, s[14:15]
	v_cndmask_b32_e64 v143, -1, v143, s[12:13]
	v_cndmask_b32_e64 v150, -1, v150, s[12:13]
	v_and_b32_e32 v130, v143, v130
	v_and_b32_e32 v142, v150, v142
	v_and_b32_e32 v143, v177, v181
	v_and_b32_e32 v150, v176, v180
	v_cndmask_b32_e64 v143, -1, v143, s[10:11]
	v_cndmask_b32_e64 v150, -1, v150, s[10:11]
	v_and_b32_e32 v130, v143, v130
	v_and_b32_e32 v142, v150, v142
	v_and_b32_e32 v143, v175, v179
	v_and_b32_e32 v150, v174, v178
	v_cndmask_b32_e64 v143, -1, v143, s[8:9]
	v_cndmask_b32_e64 v150, -1, v150, s[8:9]
	v_and_b32_e32 v130, v143, v130
	v_and_b32_e32 v142, v150, v142
	v_and_b32_e32 v143, v173, v167
	v_and_b32_e32 v150, v172, v166
	v_cndmask_b32_e64 v143, 1, v143, s[6:7]
	v_cndmask_b32_e64 v150, 1, v150, s[6:7]
	v_and_b32_e32 v130, v143, v130
	v_and_b32_e32 v142, v150, v142
	v_and_b32_e32 v143, v171, v165
	v_and_b32_e32 v150, v170, v164
	v_cndmask_b32_e64 v143, 1, v143, s[4:5]
	v_cndmask_b32_e64 v150, 1, v150, s[4:5]
	v_and_b32_e32 v130, v143, v130
	v_and_b32_e32 v142, v150, v142
	v_and_b32_e32 v143, v169, v163
	v_and_b32_e32 v150, v168, v162
	v_cndmask_b32_e64 v143, 1, v143, s[2:3]
	v_cndmask_b32_e64 v150, 1, v150, s[2:3]
	v_and_b32_e32 v130, v143, v130
	v_and_b32_e32 v142, v150, v142
	v_and_b32_e32 v143, v145, v161
	v_and_b32_e32 v150, v144, v160
	v_cndmask_b32_e32 v143, 1, v143, vcc
	v_cndmask_b32_e32 v150, 1, v150, vcc
	v_and_b32_e32 v130, v143, v130
	v_and_b32_e32 v142, v150, v142
	v_and_b32_e32 v143, 1, v130
	v_and_b32_e32 v142, 1, v142
	v_cmp_ne_u64_e64 s[16:17], s[24:25], v[142:143]
	s_and_saveexec_b64 s[30:31], s[16:17]
	s_cbranch_execz .LBB1_21
	s_add_i32 s35, s35, -1
	s_cmp_eq_u32 s35, 0
	s_cselect_b64 s[16:17], -1, 0
	s_andn2_b64 s[28:29], s[28:29], exec
	s_and_b64 s[16:17], s[16:17], exec
	s_or_b64 s[28:29], s[28:29], s[16:17]
	s_sleep 8
	s_branch .LBB1_21

.LBB1_27:
	v_mov_b64_e32 v[158:159], v[192:193]
	global_load_dwordx2 v[196:197], v[186:187], off sc1
	global_load_dwordx2 v[200:201], v[190:191], off sc1
	flat_load_dwordx2 v[194:195], v[158:159] sc1
	flat_load_dwordx2 v[198:199], v[158:159] offset:256 sc1
	v_lshl_add_u64 v[158:159], v[158:159], 0, s[24:25]
	flat_load_dwordx2 v[188:189], v[158:159] sc1
	flat_load_dwordx2 v[182:183], v[158:159] offset:256 sc1
	v_lshl_add_u64 v[158:159], v[158:159], 0, s[24:25]
	flat_load_dwordx2 v[184:185], v[158:159] sc1
	flat_load_dwordx2 v[180:181], v[158:159] offset:256 sc1
	v_lshl_add_u64 v[158:159], v[158:159], 0, s[24:25]
	flat_load_dwordx2 v[172:173], v[158:159] sc1
	flat_load_dwordx2 v[178:179], v[158:159] offset:256 sc1
	v_lshl_add_u64 v[158:159], v[158:159], 0, s[24:25]
	flat_load_dwordx2 v[170:171], v[158:159] sc1
	flat_load_dwordx2 v[176:177], v[158:159] offset:256 sc1
	v_lshl_add_u64 v[158:159], v[158:159], 0, s[24:25]
	flat_load_dwordx2 v[168:169], v[158:159] sc1
	flat_load_dwordx2 v[174:175], v[158:159] offset:256 sc1
	v_lshl_add_u64 v[206:207], v[158:159], 0, s[24:25]
	flat_load_dwordx2 v[166:167], v[206:207] sc1
	flat_load_dwordx2 v[158:159], v[206:207] offset:256 sc1
	v_lshl_add_u64 v[206:207], v[206:207], 0, s[24:25]
	s_or_b64 s[28:29], s[28:29], exec
	s_waitcnt vmcnt(0)
	v_and_b32_e32 v0, v201, v197
	v_and_b32_e32 v130, v200, v196
	s_waitcnt lgkmcnt(0)
	v_and_b32_e32 v205, v199, v195
	v_and_b32_e32 v206, v198, v194
	v_cndmask_b32_e64 v0, -1, v0, s[14:15]
	v_cndmask_b32_e64 v130, -1, v130, s[14:15]
	v_cndmask_b32_e64 v205, -1, v205, s[12:13]
	v_cndmask_b32_e64 v206, -1, v206, s[12:13]
	v_and_b32_e32 v0, v205, v0
	v_and_b32_e32 v130, v206, v130
	v_and_b32_e32 v205, v183, v189
	v_and_b32_e32 v206, v182, v188
	v_cndmask_b32_e64 v205, -1, v205, s[10:11]
	v_cndmask_b32_e64 v206, -1, v206, s[10:11]
	v_and_b32_e32 v0, v205, v0
	v_and_b32_e32 v130, v206, v130
	v_and_b32_e32 v205, v181, v185
	v_and_b32_e32 v206, v180, v184
	v_cndmask_b32_e64 v205, -1, v205, s[8:9]
	v_cndmask_b32_e64 v206, -1, v206, s[8:9]
	v_and_b32_e32 v0, v205, v0
	v_and_b32_e32 v130, v206, v130
	v_and_b32_e32 v205, v179, v173
	v_and_b32_e32 v206, v178, v172
	v_cndmask_b32_e64 v205, 1, v205, s[6:7]
	v_cndmask_b32_e64 v206, 1, v206, s[6:7]
	v_and_b32_e32 v0, v205, v0
	v_and_b32_e32 v130, v206, v130
	v_and_b32_e32 v205, v177, v171
	v_and_b32_e32 v206, v176, v170
	v_cndmask_b32_e64 v205, 1, v205, s[4:5]
	v_cndmask_b32_e64 v206, 1, v206, s[4:5]
	v_and_b32_e32 v0, v205, v0
	v_and_b32_e32 v130, v206, v130
	v_and_b32_e32 v205, v175, v169
	v_and_b32_e32 v206, v174, v168
	v_cndmask_b32_e64 v205, 1, v205, s[2:3]
	v_cndmask_b32_e64 v206, 1, v206, s[2:3]
	v_and_b32_e32 v0, v205, v0
	v_and_b32_e32 v130, v206, v130
	v_and_b32_e32 v205, v159, v167
	v_and_b32_e32 v206, v158, v166
	v_cndmask_b32_e32 v205, 1, v205, vcc
	v_cndmask_b32_e32 v206, 1, v206, vcc
	v_and_b32_e32 v0, v205, v0
	v_and_b32_e32 v130, v206, v130
	v_and_b32_e32 v207, 1, v0
	v_and_b32_e32 v206, 1, v130
	v_cmp_ne_u64_e64 s[16:17], s[26:27], v[206:207]
	s_and_saveexec_b64 s[30:31], s[16:17]
	s_cbranch_execz .LBB1_26
	s_add_i32 s35, s35, -1
	s_cmp_eq_u32 s35, 0
	s_cselect_b64 s[16:17], -1, 0
	s_andn2_b64 s[28:29], s[28:29], exec
	s_and_b64 s[16:17], s[16:17], exec
	s_or_b64 s[28:29], s[28:29], s[16:17]
	s_sleep 8
	s_branch .LBB1_26
